# combine: 16 expert-row loads in flight per row (was one at a time) + residual-row cache touch; bit-identical sums
# speedup vs baseline: 1.0226x; 1.0226x over previous
.LBB0_1149:
	v_mov_b32_e32 v1, 0x27ff0
	v_mov_b32_e32 v8, v0
	v_add_u32_e32 v1, 0, v1
	ds_read2_b32 v[2:3], v1 offset1:1
	ds_read2_b32 v[4:5], v1 offset0:2 offset1:3
	s_waitcnt lgkmcnt(0)
	s_barrier
	s_load_dword s61, s[16:17], 0x0
	s_cmp_eq_u32 s53, 0
	v_readfirstlane_b32 s4, v8
	s_cselect_b64 s[2:3], -1, 0
	s_ashr_i32 s54, s4, 6
	s_ashr_i32 s4, s4, 8
	v_and_b32_e32 v9, 31, v8
	v_bfe_u32 v1, v8, 3, 3
	v_bfe_u32 v10, v8, 5, 1
	v_lshl_or_b32 v6, s54, 3, v1
	v_lshlrev_b32_e32 v1, 7, v9
	v_lshrrev_b32_e32 v7, 1, v8
	s_waitcnt lgkmcnt(0)
	s_cmpk_lg_i32 s61, 0x100
	v_lshl_or_b32 v1, s4, 12, v1
	v_bfe_u32 v12, v8, 1, 3
	v_bitop3_b32 v7, v10, v7, 7 bitop3:0x78
	s_cselect_b64 s[22:23], -1, 0
	s_lshl_b32 s6, s54, 1
	v_lshl_or_b32 v111, v7, 4, v1
	v_bitop3_b32 v7, v10, v12, 2 bitop3:0x36
	v_readfirstlane_b32 s55, v2
	s_and_b32 s62, s6, 6
	v_bfe_u32 v2, v8, 4, 1
	v_lshl_or_b32 v112, v7, 4, v1
	v_bitop3_b32 v7, v10, v12, 4 bitop3:0x36
	v_or_b32_e32 v115, s62, v2
	v_lshlrev_b32_e32 v2, 7, v8
	v_lshrrev_b32_e32 v11, 1, v6
	v_lshl_or_b32 v113, v7, 4, v1
	v_bitop3_b32 v7, v10, v12, 6 bitop3:0x36
	v_and_b32_e32 v94, 0x780, v2
	v_lshl_or_b32 v114, v7, 4, v1
	v_readfirstlane_b32 s56, v3
	v_xor_b32_e32 v1, v11, v8
	v_lshl_add_u64 v[2:3], s[72:73], 0, v[94:95]
	v_lshlrev_b32_e32 v94, 4, v10
	v_ashrrev_i32_e32 v7, 31, v6
	s_lshl_b32 s7, s54, 12
	v_lshl_add_u64 v[96:97], v[2:3], 0, v[94:95]
	v_lshlrev_b64 v[2:3], 7, v[6:7]
	v_lshlrev_b32_e32 v1, 4, v1
	s_add_i32 s63, s7, 0
	s_mul_i32 s8, s54, 0xfffff400
	v_readfirstlane_b32 s57, v4
	v_readfirstlane_b32 s60, v5
	v_lshl_add_u64 v[4:5], s[78:79], 0, v[2:3]
	v_and_b32_e32 v6, 0x70, v1
	v_mov_b32_e32 v7, v95
	s_lshl_b32 s6, s4, 6
	s_add_i32 s10, s63, s8
	s_lshl_b32 s4, s4, 5
	s_or_b64 s[24:25], s[2:3], s[82:83]
	s_lshl_b32 s2, s54, 9
	v_and_b32_e32 v110, 63, v8
	v_lshl_add_u64 v[98:99], v[4:5], 0, v[6:7]
	s_sub_i32 s52, s10, s2
	v_lshlrev_b64 v[4:5], v8, -1
	s_add_i32 s2, s4, 0xc0
	v_not_b32_e32 v1, v5
	v_not_b32_e32 v100, v4
	v_lshlrev_b32_e32 v4, 3, v110
	v_mov_b32_e32 v5, v95
	v_lshl_add_u64 v[104:105], s[76:77], 0, v[94:95]
	v_or_b32_e32 v94, s2, v9
	s_lshl_b32 s2, s54, 13
	v_lshl_add_u64 v[102:103], s[80:81], 0, v[4:5]
	v_bitop3_b32 v5, v11, 7, v8 bitop3:0x48
	s_and_b32 s2, s2, 0x6000
	v_lshl_or_b32 v2, v5, 4, v2
	s_add_i32 s6, s6, s2
	v_lshl_add_u64 v[106:107], s[46:47], 0, v[2:3]
	v_lshl_add_u32 v2, v10, 12, s6
	s_add_i32 s2, s4, 0x8c0
	s_lshl_b32 s7, s54, 10
	v_add_u32_e32 v118, s52, v4
	v_lshlrev_b16_e32 v119, 3, v110
	v_mul_i32_i24_e32 v4, -6, v110
	v_lshl_or_b32 v2, v9, 1, v2
	v_or_b32_e32 v251, s2, v9
	s_add_i32 s2, s4, 0x10c0
	s_addk_i32 s4, 0x18c0
	v_or_b32_e32 v116, s62, v10
	v_lshlrev_b32_e32 v117, 4, v110
	v_or_b32_e32 v120, 1, v119
	v_or_b32_e32 v121, 2, v119
	v_or_b32_e32 v122, 3, v119
	v_or_b32_e32 v123, 4, v119
	v_or_b32_e32 v124, 5, v119
	v_or_b32_e32 v125, 6, v119
	v_or_b32_e32 v126, 7, v119
	v_or_b32_e32 v152, 0x801, v119
	v_or_b32_e32 v153, 0x802, v119
	v_or_b32_e32 v154, 0x803, v119
	v_or_b32_e32 v155, 0x804, v119
	v_or_b32_e32 v156, 0x805, v119
	v_or_b32_e32 v157, 0x806, v119
	v_or_b32_e32 v158, 0x807, v119
	v_or_b32_e32 v159, 0xa00, v119
	v_or_b32_e32 v160, 0xa01, v119
	v_or_b32_e32 v161, 0xa02, v119
	v_or_b32_e32 v162, 0xa03, v119
	v_or_b32_e32 v163, 0xa04, v119
	v_or_b32_e32 v164, 0xa05, v119
	v_or_b32_e32 v165, 0xa06, v119
	v_or_b32_e32 v166, 0xa07, v119
	v_or_b32_e32 v167, 0xc00, v119
	v_or_b32_e32 v168, 0xc01, v119
	v_or_b32_e32 v169, 0xc02, v119
	v_or_b32_e32 v170, 0xc03, v119
	v_or_b32_e32 v171, 0xc04, v119
	v_or_b32_e32 v172, 0xc05, v119
	v_or_b32_e32 v173, 0xc06, v119
	v_or_b32_e32 v174, 0xc07, v119
	v_or_b32_e32 v175, 0xe00, v119
	v_or_b32_e32 v176, 0xe01, v119
	v_or_b32_e32 v177, 0xe02, v119
	v_or_b32_e32 v178, 0xe03, v119
	v_or_b32_e32 v179, 0xe04, v119
	v_or_b32_e32 v180, 0xe05, v119
	v_or_b32_e32 v181, 0xe06, v119
	v_or_b32_e32 v182, 0xe07, v119
	v_or_b32_e32 v183, 0x1000, v119
	v_or_b32_e32 v184, 0x1001, v119
	v_or_b32_e32 v185, 0x1002, v119
	v_or_b32_e32 v186, 0x1003, v119
	v_or_b32_e32 v187, 0x1004, v119
	v_or_b32_e32 v188, 0x1005, v119
	v_or_b32_e32 v189, 0x1006, v119
	v_or_b32_e32 v190, 0x1007, v119
	v_or_b32_e32 v191, 0x1200, v119
	v_or_b32_e32 v192, 0x1201, v119
	v_or_b32_e32 v193, 0x1202, v119
	v_or_b32_e32 v194, 0x1203, v119
	v_or_b32_e32 v195, 0x1204, v119
	v_or_b32_e32 v196, 0x1205, v119
	v_or_b32_e32 v197, 0x1206, v119
	v_or_b32_e32 v198, 0x1207, v119
	v_or_b32_e32 v199, 0x1400, v119
	v_or_b32_e32 v200, 0x1401, v119
	v_or_b32_e32 v201, 0x1402, v119
	v_or_b32_e32 v202, 0x1403, v119
	v_or_b32_e32 v203, 0x1404, v119
	v_or_b32_e32 v204, 0x1405, v119
	v_or_b32_e32 v205, 0x1406, v119
	v_or_b32_e32 v206, 0x1407, v119
	v_or_b32_e32 v207, 0x1600, v119
	v_or_b32_e32 v208, 0x1601, v119
	v_or_b32_e32 v209, 0x1602, v119
	v_or_b32_e32 v210, 0x1603, v119
	v_or_b32_e32 v211, 0x1604, v119
	v_or_b32_e32 v212, 0x1605, v119
	v_or_b32_e32 v213, 0x1606, v119
	v_or_b32_e32 v214, 0x1607, v119
	v_or_b32_e32 v215, 0x1800, v119
	v_or_b32_e32 v216, 0x1801, v119
	v_or_b32_e32 v217, 0x1802, v119
	v_or_b32_e32 v218, 0x1803, v119
	v_or_b32_e32 v219, 0x1804, v119
	v_or_b32_e32 v220, 0x1805, v119
	v_or_b32_e32 v221, 0x1806, v119
	v_or_b32_e32 v222, 0x1807, v119
	v_or_b32_e32 v223, 0x1a00, v119
	v_or_b32_e32 v224, 0x1a01, v119
	v_or_b32_e32 v225, 0x1a02, v119
	v_or_b32_e32 v226, 0x1a03, v119
	v_or_b32_e32 v227, 0x1a04, v119
	v_or_b32_e32 v228, 0x1a05, v119
	v_or_b32_e32 v229, 0x1a06, v119
	v_or_b32_e32 v230, 0x1a07, v119
	v_or_b32_e32 v231, 0x1c00, v119
	v_or_b32_e32 v232, 0x1c01, v119
	v_or_b32_e32 v233, 0x1c02, v119
	v_or_b32_e32 v234, 0x1c03, v119
	v_or_b32_e32 v235, 0x1c04, v119
	v_or_b32_e32 v236, 0x1c05, v119
	v_or_b32_e32 v237, 0x1c06, v119
	v_or_b32_e32 v238, 0x1c07, v119
	v_or_b32_e32 v239, 0x1e00, v119
	v_or_b32_e32 v240, 0x1e01, v119
	v_or_b32_e32 v241, 0x1e02, v119
	v_or_b32_e32 v242, 0x1e03, v119
	v_or_b32_e32 v243, 0x1e04, v119
	v_or_b32_e32 v244, 0x1e05, v119
	v_or_b32_e32 v245, 0x1e06, v119
	v_or_b32_e32 v246, 0x1e07, v119
	v_or_b32_e32 v247, 64, v110
	v_or_b32_e32 v248, 0x80, v110
	v_or_b32_e32 v249, 0xc0, v110
	s_add_i32 s20, s7, 0
	v_add_u32_e32 v139, 0, v2
	v_or_b32_e32 v252, s2, v9
	v_or_b32_e32 v138, s4, v9
	s_add_i32 s21, s10, 0x8000
	s_add_i32 s6, s10, 0xa000
	s_add_i32 s7, s10, 0xc000
	s_add_i32 s10, s10, 0xe000
	v_add_u32_e32 v128, v118, v4
	s_mov_b32 s11, s19
	s_branch .LBB0_1153

.LBB0_1159:
	s_mov_b64 s[8:9], -1
	s_and_b64 vcc, exec, s[2:3]
	s_cbranch_vccz .LBB0_1152
	s_and_b32 s13, s12, 3
	s_lshl_b32 s4, s4, 3
	s_sub_i32 s14, 0x1ff8, s4
	s_lshl_b32 s12, s13, 13
	s_add_i32 s12, s12, s14
	s_or_b32 s2, s12, s62
	s_waitcnt lgkmcnt(0)
	v_or_b32_e32 v2, s12, v115
	s_ashr_i32 s3, s2, 31
	v_ashrrev_i32_e32 v3, 31, v2
	s_lshl_b64 s[8:9], s[2:3], 6
	v_lshlrev_b64 v[2:3], 11, v[2:3]
	v_lshl_add_u64 v[6:7], v[104:105], 0, s[8:9]
	v_lshl_add_u64 v[18:19], v[96:97], 0, v[2:3]
	s_or_b32 s2, s2, 1
	global_load_dwordx4 v[2:5], v[6:7], off
	s_ashr_i32 s3, s2, 31
	global_load_dwordx4 v[6:9], v[6:7], off offset:32
	s_lshl_b64 s[2:3], s[2:3], 6
	v_lshl_add_u64 v[14:15], v[104:105], 0, s[2:3]
	global_load_dwordx4 v[10:13], v[14:15], off
	s_nop 0
	global_load_dwordx4 v[14:17], v[14:15], off offset:32
	s_nop 0
	global_load_dwordx4 v[66:69], v[18:19], off
	global_load_dwordx4 v[70:73], v[18:19], off offset:32
	global_load_dwordx4 v[74:77], v[18:19], off offset:64
	global_load_dwordx4 v[78:81], v[18:19], off offset:96
	s_sub_i32 s2, 0x21f8, s4
	s_lshl_b32 s18, s13, 20
	s_add_i32 s13, s14, s54
	s_ashr_i32 s2, s2, 8
	s_add_i32 s3, s13, 0x200
	v_or_b32_e32 v129, s14, v116
	s_and_b32 s4, s2, -2
	s_ashr_i32 s14, s3, 9
	v_lshl_add_u64 v[108:109], v[98:99], 0, s[18:19]
	s_cmp_lt_i32 s2, 2
	v_mov_b32_e32 v53, 0
	s_waitcnt vmcnt(0)
	v_cvt_pk_f16_f32 v134, v10, v11
	v_cvt_pk_f16_f32 v130, v2, v3
	v_cvt_pk_f16_f32 v131, v4, v5
	v_cvt_pk_f16_f32 v132, v6, v7
	v_cvt_pk_f16_f32 v133, v8, v9
	v_cvt_pk_f16_f32 v135, v12, v13
	s_waitcnt vmcnt(4)
	v_cvt_pk_f16_f32 v136, v14, v15
	v_cvt_pk_f16_f32 v137, v16, v17
	s_cbranch_scc1 .LBB0_1177
	s_mov_b32 m0, s21
	s_waitcnt lgkmcnt(0)
	s_barrier
	s_mov_b64 s[2:3], 0x2000
	global_load_lds_dwordx4 v[108:109], off
	v_lshl_add_u64 v[2:3], v[108:109], 0, s[2:3]
	s_mov_b32 m0, s6
	s_mov_b64 s[2:3], 0x4000
	global_load_lds_dwordx4 v[2:3], off
	v_lshl_add_u64 v[2:3], v[108:109], 0, s[2:3]
	s_mov_b32 m0, s7
	s_mov_b64 s[2:3], 0x6000
	global_load_lds_dwordx4 v[2:3], off
	v_lshl_add_u64 v[2:3], v[108:109], 0, s[2:3]
	s_mov_b32 m0, s10
	s_mov_b64 s[2:3], 0x8000
	global_load_lds_dwordx4 v[2:3], off
	v_lshl_add_u64 v[2:3], v[108:109], 0, s[2:3]
	s_add_i32 m0, s20, 0x10000
	s_mov_b64 s[2:3], 0xa000
	global_load_lds_dwordx4 v[2:3], off
	v_lshl_add_u64 v[2:3], v[108:109], 0, s[2:3]
	s_add_i32 m0, s20, 0x12000
	s_mov_b64 s[2:3], 0xc000
	global_load_lds_dwordx4 v[2:3], off
	v_lshl_add_u64 v[2:3], v[108:109], 0, s[2:3]
	s_add_i32 m0, s20, 0x14000
	s_mov_b64 s[2:3], 0xe000
	global_load_lds_dwordx4 v[2:3], off
	v_lshl_add_u64 v[2:3], v[108:109], 0, s[2:3]
	s_add_i32 m0, s20, 0x16000
	s_cmp_lt_u32 s4, 3
	global_load_lds_dwordx4 v[2:3], off
	s_mov_b64 s[2:3], -1
	s_cbranch_scc0 .LBB0_1163
	s_waitcnt vmcnt(4)
	s_mov_b64 s[2:3], 0

.LBB0_1169:
	s_add_i32 s26, s15, 0
	v_add_u32_e32 v45, s26, v114
	v_add_u32_e32 v42, s26, v111
	v_add_u32_e32 v43, s26, v112
	v_add_u32_e32 v44, s26, v113
	ds_read_b128 v[34:37], v45 offset:32768
	ds_read_b128 v[18:21], v44 offset:32768
	ds_read_b128 v[22:25], v43 offset:32768
	ds_read_b128 v[2:5], v42 offset:32768
	s_mov_b64 s[26:27], -1
	s_waitcnt lgkmcnt(0)
	s_nop 0
	v_mfma_f32_32x32x16_bf16 v[2:17], v[66:69], v[2:5], 0
	v_mfma_f32_32x32x16_bf16 v[2:17], v[70:73], v[22:25], v[2:17]
	v_mfma_f32_32x32x16_bf16 v[2:17], v[74:77], v[18:21], v[2:17]
	ds_read_b128 v[18:21], v45 offset:40960
	ds_read_b128 v[22:25], v44 offset:40960
	ds_read_b128 v[26:29], v43 offset:40960
	ds_read_b128 v[38:41], v42 offset:40960
	s_waitcnt lgkmcnt(0)
	v_mfma_f32_32x32x16_bf16 v[2:17], v[78:81], v[34:37], v[2:17]
	v_mov_b32_e32 v34, 0
	v_mov_b32_e32 v35, 0
	s_nop 9
	v_cvt_pkrtz_f16_f32 v2, v2, v3
	v_cvt_pkrtz_f16_f32 v3, v10, v11
	v_pk_max_i16 v2, v2, 0
	v_pk_max_i16 v3, v3, 0
	v_dot2c_f32_f16_e32 v34, v2, v130
	v_dot2c_f32_f16_e32 v35, v3, v134
	v_cvt_pkrtz_f16_f32 v2, v4, v5
	v_cvt_pkrtz_f16_f32 v3, v12, v13
	v_pk_max_i16 v2, v2, 0
	v_pk_max_i16 v3, v3, 0
	v_dot2c_f32_f16_e32 v34, v2, v131
	v_dot2c_f32_f16_e32 v35, v3, v135
	v_cvt_pkrtz_f16_f32 v2, v6, v7
	v_cvt_pkrtz_f16_f32 v3, v14, v15
	v_pk_max_i16 v2, v2, 0
	v_pk_max_i16 v3, v3, 0
	v_dot2c_f32_f16_e32 v34, v2, v132
	v_dot2c_f32_f16_e32 v35, v3, v136
	v_cvt_pkrtz_f16_f32 v2, v8, v9
	v_cvt_pkrtz_f16_f32 v3, v16, v17
	v_pk_max_i16 v2, v2, 0
	v_pk_max_i16 v3, v3, 0
	v_dot2c_f32_f16_e32 v34, v2, v133
	v_dot2c_f32_f16_e32 v35, v3, v137
	v_mfma_f32_32x32x16_bf16 v[2:17], v[66:69], v[38:41], 0
	s_nop 1
	v_permlane32_swap_b32_e32 v34, v35
	v_mfma_f32_32x32x16_bf16 v[2:17], v[70:73], v[26:29], v[2:17]
	v_mfma_f32_32x32x16_bf16 v[2:17], v[74:77], v[22:25], v[2:17]
	v_add_f32_e32 v23, v34, v35
	v_cvt_f16_f32_e32 v23, v23
	v_add_u32_e32 v22, 0xffffff40, v33
	v_cmp_le_i32_e32 vcc, v22, v129
	v_ashrrev_i16_e32 v24, 15, v23
	v_bitop3_b16 v23, v24, v23, s50 bitop3:0x36
	v_mfma_f32_32x32x16_bf16 v[2:17], v[78:81], v[18:21], v[2:17]
	v_cndmask_b32_e32 v22, 0, v23, vcc
	v_mov_b32_e32 v18, 0
	v_mov_b32_e32 v19, 0
	ds_write_b16 v32, v22
	ds_read_b128 v[22:25], v45 offset:49152
	ds_read_b128 v[26:29], v44 offset:49152
	ds_read_b128 v[34:37], v43 offset:49152
	ds_read_b128 v[38:41], v42 offset:49152
	s_waitcnt lgkmcnt(0)
	s_nop 2
	v_cvt_pkrtz_f16_f32 v2, v2, v3
	v_cvt_pkrtz_f16_f32 v3, v10, v11
	v_pk_max_i16 v2, v2, 0
	v_pk_max_i16 v3, v3, 0
	v_dot2c_f32_f16_e32 v18, v2, v130
	v_dot2c_f32_f16_e32 v19, v3, v134
	v_cvt_pkrtz_f16_f32 v2, v4, v5
	v_cvt_pkrtz_f16_f32 v3, v12, v13
	v_pk_max_i16 v2, v2, 0
	v_pk_max_i16 v3, v3, 0
	v_dot2c_f32_f16_e32 v18, v2, v131
	v_dot2c_f32_f16_e32 v19, v3, v135
	v_cvt_pkrtz_f16_f32 v2, v6, v7
	v_cvt_pkrtz_f16_f32 v3, v14, v15
	v_pk_max_i16 v2, v2, 0
	v_pk_max_i16 v3, v3, 0
	v_dot2c_f32_f16_e32 v18, v2, v132
	v_dot2c_f32_f16_e32 v19, v3, v136
	v_cvt_pkrtz_f16_f32 v2, v8, v9
	v_cvt_pkrtz_f16_f32 v3, v16, v17
	v_pk_max_i16 v2, v2, 0
	v_pk_max_i16 v3, v3, 0
	v_dot2c_f32_f16_e32 v18, v2, v133
	v_dot2c_f32_f16_e32 v19, v3, v137
	v_mfma_f32_32x32x16_bf16 v[2:17], v[66:69], v[38:41], 0
	v_add_u32_e32 v20, 0xffffff80, v33
	v_cmp_le_i32_e32 vcc, v20, v129
	v_permlane32_swap_b32_e32 v18, v19
	v_add_f32_e32 v18, v18, v19
	v_cvt_f16_f32_e32 v18, v18
	v_ashrrev_i16_e32 v19, 15, v18
	v_mfma_f32_32x32x16_bf16 v[2:17], v[70:73], v[34:37], v[2:17]
	v_bitop3_b16 v18, v19, v18, s50 bitop3:0x36
	v_cndmask_b32_e32 v18, 0, v18, vcc
	ds_write_b16 v32, v18 offset:128
	v_mfma_f32_32x32x16_bf16 v[2:17], v[74:77], v[26:29], v[2:17]
	ds_read_b128 v[18:21], v45 offset:57344
	ds_read_b128 v[26:29], v44 offset:57344
	ds_read_b128 v[34:37], v43 offset:57344
	ds_read_b128 v[38:41], v42 offset:57344
	s_waitcnt lgkmcnt(0)
	v_mfma_f32_32x32x16_bf16 v[2:17], v[78:81], v[22:25], v[2:17]
	v_mov_b32_e32 v22, 0
	v_mov_b32_e32 v23, 0
	s_nop 9
	v_cvt_pkrtz_f16_f32 v2, v2, v3
	v_cvt_pkrtz_f16_f32 v3, v10, v11
	v_pk_max_i16 v2, v2, 0
	v_pk_max_i16 v3, v3, 0
	v_dot2c_f32_f16_e32 v22, v2, v130
	v_dot2c_f32_f16_e32 v23, v3, v134
	v_cvt_pkrtz_f16_f32 v2, v4, v5
	v_cvt_pkrtz_f16_f32 v3, v12, v13
	v_pk_max_i16 v2, v2, 0
	v_pk_max_i16 v3, v3, 0
	v_dot2c_f32_f16_e32 v22, v2, v131
	v_dot2c_f32_f16_e32 v23, v3, v135
	v_cvt_pkrtz_f16_f32 v2, v6, v7
	v_cvt_pkrtz_f16_f32 v3, v14, v15
	v_pk_max_i16 v2, v2, 0
	v_pk_max_i16 v3, v3, 0
	v_dot2c_f32_f16_e32 v22, v2, v132
	v_dot2c_f32_f16_e32 v23, v3, v136
	v_cvt_pkrtz_f16_f32 v2, v8, v9
	v_cvt_pkrtz_f16_f32 v3, v16, v17
	v_pk_max_i16 v2, v2, 0
	v_pk_max_i16 v3, v3, 0
	v_dot2c_f32_f16_e32 v22, v2, v133
	v_dot2c_f32_f16_e32 v23, v3, v137
	v_mfma_f32_32x32x16_bf16 v[2:17], v[66:69], v[38:41], 0
	s_nop 1
	v_permlane32_swap_b32_e32 v22, v23
	v_mfma_f32_32x32x16_bf16 v[2:17], v[70:73], v[34:37], v[2:17]
	v_mfma_f32_32x32x16_bf16 v[2:17], v[74:77], v[26:29], v[2:17]
	v_mfma_f32_32x32x16_bf16 v[2:17], v[78:81], v[18:21], v[2:17]
	v_add_f32_e32 v19, v22, v23
	v_cvt_f16_f32_e32 v19, v19
	v_subrev_u32_e32 v18, 64, v33
	v_cmp_le_i32_e32 vcc, v18, v129
	v_ashrrev_i16_e32 v20, 15, v19
	v_bitop3_b16 v19, v20, v19, s50 bitop3:0x36
	s_nop 5
	v_cvt_pkrtz_f16_f32 v2, v2, v3
	v_pk_max_i16 v2, v2, 0
	v_cvt_pkrtz_f16_f32 v3, v10, v11
	v_mov_b32_e32 v10, 0
	v_pk_max_i16 v3, v3, 0
	v_dot2c_f32_f16_e32 v10, v2, v130
	v_mov_b32_e32 v2, 0
	v_dot2c_f32_f16_e32 v2, v3, v134
	v_cvt_pkrtz_f16_f32 v3, v4, v5
	v_cvt_pkrtz_f16_f32 v4, v12, v13
	v_pk_max_i16 v3, v3, 0
	v_pk_max_i16 v4, v4, 0
	v_dot2c_f32_f16_e32 v10, v3, v131
	v_dot2c_f32_f16_e32 v2, v4, v135
	v_cvt_pkrtz_f16_f32 v3, v6, v7
	v_cvt_pkrtz_f16_f32 v4, v14, v15
	v_pk_max_i16 v3, v3, 0
	v_pk_max_i16 v4, v4, 0
	v_dot2c_f32_f16_e32 v10, v3, v132
	v_dot2c_f32_f16_e32 v2, v4, v136
	v_cvt_pkrtz_f16_f32 v3, v8, v9
	v_cvt_pkrtz_f16_f32 v4, v16, v17
	v_pk_max_i16 v3, v3, 0
	v_pk_max_i16 v4, v4, 0
	v_dot2c_f32_f16_e32 v10, v3, v133
	v_dot2c_f32_f16_e32 v2, v4, v137
	v_cndmask_b32_e32 v18, 0, v19, vcc
	v_cmp_le_i32_e32 vcc, v33, v129
	ds_write_b16 v32, v18 offset:256
	v_permlane32_swap_b32_e32 v10, v2
	v_add_f32_e32 v2, v10, v2
	v_cvt_f16_f32_e32 v2, v2
	v_ashrrev_i16_e32 v3, 15, v2
	v_bitop3_b16 v2, v3, v2, s50 bitop3:0x36
	v_cndmask_b32_e32 v2, 0, v2, vcc
	s_and_b64 vcc, exec, s[8:9]
	ds_write_b16 v32, v2 offset:384
	s_cbranch_vccz .LBB0_1175
	s_cmp_lg_u32 s28, 2
	s_mov_b64 s[8:9], -1
	s_cbranch_scc0 .LBB0_1172
	s_waitcnt vmcnt(0) lgkmcnt(0)
	s_mov_b64 s[8:9], 0

.LBB0_1191:
	s_add_i32 s3, s28, 0
	v_add_u32_e32 v59, s3, v114
	v_add_u32_e32 v48, s3, v111
	v_add_u32_e32 v49, s3, v112
	v_add_u32_e32 v58, s3, v113
	ds_read_b128 v[44:47], v59 offset:32768
	ds_read_b128 v[22:25], v58 offset:32768
	ds_read_b128 v[30:33], v49 offset:32768
	ds_read_b128 v[2:5], v48 offset:32768
	s_mov_b64 s[26:27], -1
	s_waitcnt lgkmcnt(0)
	s_nop 0
	v_mfma_f32_32x32x16_bf16 v[2:17], v[66:69], v[2:5], 0
	v_mfma_f32_32x32x16_bf16 v[2:17], v[70:73], v[30:33], v[2:17]
	v_mfma_f32_32x32x16_bf16 v[2:17], v[74:77], v[22:25], v[2:17]
	ds_read_b128 v[22:25], v59 offset:40960
	ds_read_b128 v[30:33], v58 offset:40960
	ds_read_b128 v[34:37], v49 offset:40960
	ds_read_b128 v[54:57], v48 offset:40960
	s_waitcnt lgkmcnt(0)
	v_mfma_f32_32x32x16_bf16 v[2:17], v[78:81], v[44:47], v[2:17]
	v_mov_b32_e32 v44, 0
	v_mov_b32_e32 v45, 0
	s_nop 9
	v_cvt_pkrtz_f16_f32 v2, v2, v3
	v_cvt_pkrtz_f16_f32 v3, v10, v11
	v_pk_max_i16 v2, v2, 0
	v_pk_max_i16 v3, v3, 0
	v_dot2c_f32_f16_e32 v44, v2, v130
	v_dot2c_f32_f16_e32 v45, v3, v134
	v_cvt_pkrtz_f16_f32 v2, v4, v5
	v_cvt_pkrtz_f16_f32 v3, v12, v13
	v_pk_max_i16 v2, v2, 0
	v_pk_max_i16 v3, v3, 0
	v_dot2c_f32_f16_e32 v44, v2, v131
	v_dot2c_f32_f16_e32 v45, v3, v135
	v_cvt_pkrtz_f16_f32 v2, v6, v7
	v_cvt_pkrtz_f16_f32 v3, v14, v15
	v_pk_max_i16 v2, v2, 0
	v_pk_max_i16 v3, v3, 0
	v_dot2c_f32_f16_e32 v44, v2, v132
	v_dot2c_f32_f16_e32 v45, v3, v136
	v_cvt_pkrtz_f16_f32 v2, v8, v9
	v_cvt_pkrtz_f16_f32 v3, v16, v17
	v_pk_max_i16 v2, v2, 0
	v_pk_max_i16 v3, v3, 0
	v_dot2c_f32_f16_e32 v44, v2, v133
	v_dot2c_f32_f16_e32 v45, v3, v137
	v_mfma_f32_32x32x16_bf16 v[2:17], v[66:69], v[54:57], 0
	s_nop 1
	v_permlane32_swap_b32_e32 v44, v45
	v_mfma_f32_32x32x16_bf16 v[2:17], v[70:73], v[34:37], v[2:17]
	v_mfma_f32_32x32x16_bf16 v[2:17], v[74:77], v[30:33], v[2:17]
	v_add_f32_e32 v31, v44, v45
	v_cvt_f16_f32_e32 v31, v31
	v_add_u32_e32 v30, 0xffffff40, v42
	v_cmp_le_i32_e32 vcc, v30, v129
	v_ashrrev_i16_e32 v32, 15, v31
	v_bitop3_b16 v31, v32, v31, s50 bitop3:0x36
	v_mfma_f32_32x32x16_bf16 v[2:17], v[78:81], v[22:25], v[2:17]
	v_cndmask_b32_e32 v30, 0, v31, vcc
	v_mov_b32_e32 v22, 0
	v_mov_b32_e32 v23, 0
	ds_write_b16 v43, v30
	ds_read_b128 v[30:33], v59 offset:49152
	ds_read_b128 v[34:37], v58 offset:49152
	ds_read_b128 v[44:47], v49 offset:49152
	ds_read_b128 v[54:57], v48 offset:49152
	s_waitcnt lgkmcnt(0)
	s_nop 2
	v_cvt_pkrtz_f16_f32 v2, v2, v3
	v_cvt_pkrtz_f16_f32 v3, v10, v11
	v_pk_max_i16 v2, v2, 0
	v_pk_max_i16 v3, v3, 0
	v_dot2c_f32_f16_e32 v22, v2, v130
	v_dot2c_f32_f16_e32 v23, v3, v134
	v_cvt_pkrtz_f16_f32 v2, v4, v5
	v_cvt_pkrtz_f16_f32 v3, v12, v13
	v_pk_max_i16 v2, v2, 0
	v_pk_max_i16 v3, v3, 0
	v_dot2c_f32_f16_e32 v22, v2, v131
	v_dot2c_f32_f16_e32 v23, v3, v135
	v_cvt_pkrtz_f16_f32 v2, v6, v7
	v_cvt_pkrtz_f16_f32 v3, v14, v15
	v_pk_max_i16 v2, v2, 0
	v_pk_max_i16 v3, v3, 0
	v_dot2c_f32_f16_e32 v22, v2, v132
	v_dot2c_f32_f16_e32 v23, v3, v136
	v_cvt_pkrtz_f16_f32 v2, v8, v9
	v_cvt_pkrtz_f16_f32 v3, v16, v17
	v_pk_max_i16 v2, v2, 0
	v_pk_max_i16 v3, v3, 0
	v_dot2c_f32_f16_e32 v22, v2, v133
	v_dot2c_f32_f16_e32 v23, v3, v137
	v_mfma_f32_32x32x16_bf16 v[2:17], v[66:69], v[54:57], 0
	v_add_u32_e32 v24, 0xffffff80, v42
	v_cmp_le_i32_e32 vcc, v24, v129
	v_permlane32_swap_b32_e32 v22, v23
	v_add_f32_e32 v22, v22, v23
	v_cvt_f16_f32_e32 v22, v22
	v_ashrrev_i16_e32 v23, 15, v22
	v_mfma_f32_32x32x16_bf16 v[2:17], v[70:73], v[44:47], v[2:17]
	v_bitop3_b16 v22, v23, v22, s50 bitop3:0x36
	v_cndmask_b32_e32 v22, 0, v22, vcc
	ds_write_b16 v43, v22 offset:128
	v_mfma_f32_32x32x16_bf16 v[2:17], v[74:77], v[34:37], v[2:17]
	ds_read_b128 v[22:25], v59 offset:57344
	ds_read_b128 v[34:37], v58 offset:57344
	ds_read_b128 v[44:47], v49 offset:57344
	ds_read_b128 v[54:57], v48 offset:57344
	s_waitcnt lgkmcnt(0)
	v_mfma_f32_32x32x16_bf16 v[2:17], v[78:81], v[30:33], v[2:17]
	v_mov_b32_e32 v30, 0
	v_mov_b32_e32 v31, 0
	s_nop 9
	v_cvt_pkrtz_f16_f32 v2, v2, v3
	v_cvt_pkrtz_f16_f32 v3, v10, v11
	v_pk_max_i16 v2, v2, 0
	v_pk_max_i16 v3, v3, 0
	v_dot2c_f32_f16_e32 v30, v2, v130
	v_dot2c_f32_f16_e32 v31, v3, v134
	v_cvt_pkrtz_f16_f32 v2, v4, v5
	v_cvt_pkrtz_f16_f32 v3, v12, v13
	v_pk_max_i16 v2, v2, 0
	v_pk_max_i16 v3, v3, 0
	v_dot2c_f32_f16_e32 v30, v2, v131
	v_dot2c_f32_f16_e32 v31, v3, v135
	v_cvt_pkrtz_f16_f32 v2, v6, v7
	v_cvt_pkrtz_f16_f32 v3, v14, v15
	v_pk_max_i16 v2, v2, 0
	v_pk_max_i16 v3, v3, 0
	v_dot2c_f32_f16_e32 v30, v2, v132
	v_dot2c_f32_f16_e32 v31, v3, v136
	v_cvt_pkrtz_f16_f32 v2, v8, v9
	v_cvt_pkrtz_f16_f32 v3, v16, v17
	v_pk_max_i16 v2, v2, 0
	v_pk_max_i16 v3, v3, 0
	v_dot2c_f32_f16_e32 v30, v2, v133
	v_dot2c_f32_f16_e32 v31, v3, v137
	v_mfma_f32_32x32x16_bf16 v[2:17], v[66:69], v[54:57], 0
	s_nop 1
	v_permlane32_swap_b32_e32 v30, v31
	v_mfma_f32_32x32x16_bf16 v[2:17], v[70:73], v[44:47], v[2:17]
	v_mfma_f32_32x32x16_bf16 v[2:17], v[74:77], v[34:37], v[2:17]
	v_mfma_f32_32x32x16_bf16 v[2:17], v[78:81], v[22:25], v[2:17]
	v_add_f32_e32 v23, v30, v31
	v_cvt_f16_f32_e32 v23, v23
	v_subrev_u32_e32 v22, 64, v42
	v_cmp_le_i32_e32 vcc, v22, v129
	v_ashrrev_i16_e32 v24, 15, v23
	v_bitop3_b16 v23, v24, v23, s50 bitop3:0x36
	s_nop 5
	v_cvt_pkrtz_f16_f32 v2, v2, v3
	v_pk_max_i16 v2, v2, 0
	v_cvt_pkrtz_f16_f32 v3, v10, v11
	v_mov_b32_e32 v10, 0
	v_pk_max_i16 v3, v3, 0
	v_dot2c_f32_f16_e32 v10, v2, v130
	v_mov_b32_e32 v2, 0
	v_dot2c_f32_f16_e32 v2, v3, v134
	v_cvt_pkrtz_f16_f32 v3, v4, v5
	v_cvt_pkrtz_f16_f32 v4, v12, v13
	v_pk_max_i16 v3, v3, 0
	v_pk_max_i16 v4, v4, 0
	v_dot2c_f32_f16_e32 v10, v3, v131
	v_dot2c_f32_f16_e32 v2, v4, v135
	v_cvt_pkrtz_f16_f32 v3, v6, v7
	v_cvt_pkrtz_f16_f32 v4, v14, v15
	v_pk_max_i16 v3, v3, 0
	v_pk_max_i16 v4, v4, 0
	v_dot2c_f32_f16_e32 v10, v3, v132
	v_dot2c_f32_f16_e32 v2, v4, v136
	v_cvt_pkrtz_f16_f32 v3, v8, v9
	v_cvt_pkrtz_f16_f32 v4, v16, v17
	v_pk_max_i16 v3, v3, 0
	v_pk_max_i16 v4, v4, 0
	v_dot2c_f32_f16_e32 v10, v3, v133
	v_dot2c_f32_f16_e32 v2, v4, v137
	v_cndmask_b32_e32 v22, 0, v23, vcc
	v_cmp_le_i32_e32 vcc, v42, v129
	ds_write_b16 v43, v22 offset:256
	v_permlane32_swap_b32_e32 v10, v2
	v_add_f32_e32 v2, v10, v2
	v_cvt_f16_f32_e32 v2, v2
	v_ashrrev_i16_e32 v3, 15, v2
	v_bitop3_b16 v2, v3, v2, s50 bitop3:0x36
	v_cndmask_b32_e32 v2, 0, v2, vcc
	s_and_b64 vcc, exec, s[8:9]
	ds_write_b16 v43, v2 offset:384
	s_cbranch_vccz .LBB0_1196
	s_cmp_lg_u32 s18, 0
	s_cbranch_scc0 .LBB0_1198
	s_waitcnt vmcnt(0) lgkmcnt(0)
	s_cbranch_execnz .LBB0_1195

.LBB0_1213:
	s_add_i32 s3, s28, 0
	v_add_u32_e32 v91, s3, v114
	v_add_u32_e32 v64, s3, v111
	v_add_u32_e32 v65, s3, v112
	v_add_u32_e32 v90, s3, v113
	ds_read_b128 v[82:85], v91 offset:32768
	ds_read_b128 v[30:33], v90 offset:32768
	ds_read_b128 v[42:45], v65 offset:32768
	ds_read_b128 v[2:5], v64 offset:32768
	s_mov_b64 s[26:27], -1
	s_waitcnt lgkmcnt(0)
	s_nop 0
	v_mfma_f32_32x32x16_bf16 v[2:17], v[66:69], v[2:5], 0
	v_mfma_f32_32x32x16_bf16 v[2:17], v[70:73], v[42:45], v[2:17]
	v_mfma_f32_32x32x16_bf16 v[2:17], v[74:77], v[30:33], v[2:17]
	ds_read_b128 v[30:33], v91 offset:40960
	ds_read_b128 v[42:45], v90 offset:40960
	ds_read_b128 v[54:57], v65 offset:40960
	ds_read_b128 v[86:89], v64 offset:40960
	s_waitcnt lgkmcnt(0)
	v_mfma_f32_32x32x16_bf16 v[2:17], v[78:81], v[82:85], v[2:17]
	v_mov_b32_e32 v82, 0
	v_mov_b32_e32 v83, 0
	s_nop 9
	v_cvt_pkrtz_f16_f32 v2, v2, v3
	v_cvt_pkrtz_f16_f32 v3, v10, v11
	v_pk_max_i16 v2, v2, 0
	v_pk_max_i16 v3, v3, 0
	v_dot2c_f32_f16_e32 v82, v2, v130
	v_dot2c_f32_f16_e32 v83, v3, v134
	v_cvt_pkrtz_f16_f32 v2, v4, v5
	v_cvt_pkrtz_f16_f32 v3, v12, v13
	v_pk_max_i16 v2, v2, 0
	v_pk_max_i16 v3, v3, 0
	v_dot2c_f32_f16_e32 v82, v2, v131
	v_dot2c_f32_f16_e32 v83, v3, v135
	v_cvt_pkrtz_f16_f32 v2, v6, v7
	v_cvt_pkrtz_f16_f32 v3, v14, v15
	v_pk_max_i16 v2, v2, 0
	v_pk_max_i16 v3, v3, 0
	v_dot2c_f32_f16_e32 v82, v2, v132
	v_dot2c_f32_f16_e32 v83, v3, v136
	v_cvt_pkrtz_f16_f32 v2, v8, v9
	v_cvt_pkrtz_f16_f32 v3, v16, v17
	v_pk_max_i16 v2, v2, 0
	v_pk_max_i16 v3, v3, 0
	v_dot2c_f32_f16_e32 v82, v2, v133
	v_dot2c_f32_f16_e32 v83, v3, v137
	v_mfma_f32_32x32x16_bf16 v[2:17], v[66:69], v[86:89], 0
	s_nop 1
	v_permlane32_swap_b32_e32 v82, v83
	v_mfma_f32_32x32x16_bf16 v[2:17], v[70:73], v[54:57], v[2:17]
	v_mfma_f32_32x32x16_bf16 v[2:17], v[74:77], v[42:45], v[2:17]
	v_add_f32_e32 v43, v82, v83
	v_cvt_f16_f32_e32 v43, v43
	v_add_u32_e32 v42, 0xffffff40, v62
	v_cmp_le_i32_e32 vcc, v42, v129
	v_ashrrev_i16_e32 v44, 15, v43
	v_bitop3_b16 v43, v44, v43, s50 bitop3:0x36
	v_mfma_f32_32x32x16_bf16 v[2:17], v[78:81], v[30:33], v[2:17]
	v_cndmask_b32_e32 v42, 0, v43, vcc
	v_mov_b32_e32 v30, 0
	v_mov_b32_e32 v31, 0
	ds_write_b16 v63, v42
	ds_read_b128 v[42:45], v91 offset:49152
	ds_read_b128 v[54:57], v90 offset:49152
	ds_read_b128 v[82:85], v65 offset:49152
	ds_read_b128 v[86:89], v64 offset:49152
	s_waitcnt lgkmcnt(0)
	s_nop 2
	v_cvt_pkrtz_f16_f32 v2, v2, v3
	v_cvt_pkrtz_f16_f32 v3, v10, v11
	v_pk_max_i16 v2, v2, 0
	v_pk_max_i16 v3, v3, 0
	v_dot2c_f32_f16_e32 v30, v2, v130
	v_dot2c_f32_f16_e32 v31, v3, v134
	v_cvt_pkrtz_f16_f32 v2, v4, v5
	v_cvt_pkrtz_f16_f32 v3, v12, v13
	v_pk_max_i16 v2, v2, 0
	v_pk_max_i16 v3, v3, 0
	v_dot2c_f32_f16_e32 v30, v2, v131
	v_dot2c_f32_f16_e32 v31, v3, v135
	v_cvt_pkrtz_f16_f32 v2, v6, v7
	v_cvt_pkrtz_f16_f32 v3, v14, v15
	v_pk_max_i16 v2, v2, 0
	v_pk_max_i16 v3, v3, 0
	v_dot2c_f32_f16_e32 v30, v2, v132
	v_dot2c_f32_f16_e32 v31, v3, v136
	v_cvt_pkrtz_f16_f32 v2, v8, v9
	v_cvt_pkrtz_f16_f32 v3, v16, v17
	v_pk_max_i16 v2, v2, 0
	v_pk_max_i16 v3, v3, 0
	v_dot2c_f32_f16_e32 v30, v2, v133
	v_dot2c_f32_f16_e32 v31, v3, v137
	v_mfma_f32_32x32x16_bf16 v[2:17], v[66:69], v[86:89], 0
	v_add_u32_e32 v32, 0xffffff80, v62
	v_cmp_le_i32_e32 vcc, v32, v129
	v_permlane32_swap_b32_e32 v30, v31
	v_add_f32_e32 v30, v30, v31
	v_cvt_f16_f32_e32 v30, v30
	v_ashrrev_i16_e32 v31, 15, v30
	v_mfma_f32_32x32x16_bf16 v[2:17], v[70:73], v[82:85], v[2:17]
	v_bitop3_b16 v30, v31, v30, s50 bitop3:0x36
	v_cndmask_b32_e32 v30, 0, v30, vcc
	ds_write_b16 v63, v30 offset:128
	v_mfma_f32_32x32x16_bf16 v[2:17], v[74:77], v[54:57], v[2:17]
	ds_read_b128 v[30:33], v91 offset:57344
	ds_read_b128 v[54:57], v90 offset:57344
	ds_read_b128 v[82:85], v65 offset:57344
	ds_read_b128 v[86:89], v64 offset:57344
	s_waitcnt lgkmcnt(0)
	v_mfma_f32_32x32x16_bf16 v[2:17], v[78:81], v[42:45], v[2:17]
	v_mov_b32_e32 v42, 0
	v_mov_b32_e32 v43, 0
	s_nop 9
	v_cvt_pkrtz_f16_f32 v2, v2, v3
	v_cvt_pkrtz_f16_f32 v3, v10, v11
	v_pk_max_i16 v2, v2, 0
	v_pk_max_i16 v3, v3, 0
	v_dot2c_f32_f16_e32 v42, v2, v130
	v_dot2c_f32_f16_e32 v43, v3, v134
	v_cvt_pkrtz_f16_f32 v2, v4, v5
	v_cvt_pkrtz_f16_f32 v3, v12, v13
	v_pk_max_i16 v2, v2, 0
	v_pk_max_i16 v3, v3, 0
	v_dot2c_f32_f16_e32 v42, v2, v131
	v_dot2c_f32_f16_e32 v43, v3, v135
	v_cvt_pkrtz_f16_f32 v2, v6, v7
	v_cvt_pkrtz_f16_f32 v3, v14, v15
	v_pk_max_i16 v2, v2, 0
	v_pk_max_i16 v3, v3, 0
	v_dot2c_f32_f16_e32 v42, v2, v132
	v_dot2c_f32_f16_e32 v43, v3, v136
	v_cvt_pkrtz_f16_f32 v2, v8, v9
	v_cvt_pkrtz_f16_f32 v3, v16, v17
	v_pk_max_i16 v2, v2, 0
	v_pk_max_i16 v3, v3, 0
	v_dot2c_f32_f16_e32 v42, v2, v133
	v_dot2c_f32_f16_e32 v43, v3, v137
	v_mfma_f32_32x32x16_bf16 v[2:17], v[66:69], v[86:89], 0
	s_nop 1
	v_permlane32_swap_b32_e32 v42, v43
	v_mfma_f32_32x32x16_bf16 v[2:17], v[70:73], v[82:85], v[2:17]
	v_mfma_f32_32x32x16_bf16 v[2:17], v[74:77], v[54:57], v[2:17]
	v_mfma_f32_32x32x16_bf16 v[2:17], v[78:81], v[30:33], v[2:17]
	v_add_f32_e32 v31, v42, v43
	v_cvt_f16_f32_e32 v31, v31
	v_subrev_u32_e32 v30, 64, v62
	v_cmp_le_i32_e32 vcc, v30, v129
	v_ashrrev_i16_e32 v32, 15, v31
	v_bitop3_b16 v31, v32, v31, s50 bitop3:0x36
	s_nop 5
	v_cvt_pkrtz_f16_f32 v2, v2, v3
	v_pk_max_i16 v2, v2, 0
	v_cvt_pkrtz_f16_f32 v3, v10, v11
	v_mov_b32_e32 v10, 0
	v_pk_max_i16 v3, v3, 0
	v_dot2c_f32_f16_e32 v10, v2, v130
	v_mov_b32_e32 v2, 0
	v_dot2c_f32_f16_e32 v2, v3, v134
	v_cvt_pkrtz_f16_f32 v3, v4, v5
	v_cvt_pkrtz_f16_f32 v4, v12, v13
	v_pk_max_i16 v3, v3, 0
	v_pk_max_i16 v4, v4, 0
	v_dot2c_f32_f16_e32 v10, v3, v131
	v_dot2c_f32_f16_e32 v2, v4, v135
	v_cvt_pkrtz_f16_f32 v3, v6, v7
	v_cvt_pkrtz_f16_f32 v4, v14, v15
	v_pk_max_i16 v3, v3, 0
	v_pk_max_i16 v4, v4, 0
	v_dot2c_f32_f16_e32 v10, v3, v132
	v_dot2c_f32_f16_e32 v2, v4, v136
	v_cvt_pkrtz_f16_f32 v3, v8, v9
	v_cvt_pkrtz_f16_f32 v4, v16, v17
	v_pk_max_i16 v3, v3, 0
	v_pk_max_i16 v4, v4, 0
	v_dot2c_f32_f16_e32 v10, v3, v133
	v_dot2c_f32_f16_e32 v2, v4, v137
	v_cndmask_b32_e32 v30, 0, v31, vcc
	v_cmp_le_i32_e32 vcc, v62, v129
	ds_write_b16 v63, v30 offset:256
	v_permlane32_swap_b32_e32 v10, v2
	v_add_f32_e32 v2, v10, v2
	v_cvt_f16_f32_e32 v2, v2
	v_ashrrev_i16_e32 v3, 15, v2
	v_bitop3_b16 v2, v3, v2, s50 bitop3:0x36
	v_cndmask_b32_e32 v2, 0, v2, vcc
	s_and_b64 vcc, exec, s[8:9]
	ds_write_b16 v63, v2 offset:384
	s_cbranch_vccz .LBB0_1218
	s_cmp_lg_u32 s18, 0
	s_cbranch_scc0 .LBB0_1220
	s_waitcnt vmcnt(0) lgkmcnt(0)
	s_cbranch_execnz .LBB0_1217

.LBB0_1235:
	s_add_i32 s3, s18, 0
	v_add_u32_e32 v151, s3, v114
	v_add_u32_e32 v148, s3, v111
	v_add_u32_e32 v149, s3, v112
	v_add_u32_e32 v150, s3, v113
	ds_read_b128 v[140:143], v151 offset:32768
	ds_read_b128 v[82:85], v150 offset:32768
	ds_read_b128 v[86:89], v149 offset:32768
	ds_read_b128 v[2:5], v148 offset:32768
	s_mov_b64 s[26:27], -1
	s_waitcnt lgkmcnt(0)
	s_nop 0
	v_mfma_f32_32x32x16_bf16 v[2:17], v[66:69], v[2:5], 0
	v_mfma_f32_32x32x16_bf16 v[2:17], v[70:73], v[86:89], v[2:17]
	v_mfma_f32_32x32x16_bf16 v[2:17], v[74:77], v[82:85], v[2:17]
	ds_read_b128 v[82:85], v151 offset:40960
	ds_read_b128 v[86:89], v150 offset:40960
	ds_read_b128 v[90:93], v149 offset:40960
	ds_read_b128 v[144:147], v148 offset:40960
	s_waitcnt lgkmcnt(0)
	v_mfma_f32_32x32x16_bf16 v[2:17], v[78:81], v[140:143], v[2:17]
	v_mov_b32_e32 v140, 0
	v_mov_b32_e32 v141, 0
	s_nop 9
	v_cvt_pkrtz_f16_f32 v2, v2, v3
	v_cvt_pkrtz_f16_f32 v3, v10, v11
	v_pk_max_i16 v2, v2, 0
	v_pk_max_i16 v3, v3, 0
	v_dot2c_f32_f16_e32 v140, v2, v130
	v_dot2c_f32_f16_e32 v141, v3, v134
	v_cvt_pkrtz_f16_f32 v2, v4, v5
	v_cvt_pkrtz_f16_f32 v3, v12, v13
	v_pk_max_i16 v2, v2, 0
	v_pk_max_i16 v3, v3, 0
	v_dot2c_f32_f16_e32 v140, v2, v131
	v_dot2c_f32_f16_e32 v141, v3, v135
	v_cvt_pkrtz_f16_f32 v2, v6, v7
	v_cvt_pkrtz_f16_f32 v3, v14, v15
	v_pk_max_i16 v2, v2, 0
	v_pk_max_i16 v3, v3, 0
	v_dot2c_f32_f16_e32 v140, v2, v132
	v_dot2c_f32_f16_e32 v141, v3, v136
	v_cvt_pkrtz_f16_f32 v2, v8, v9
	v_cvt_pkrtz_f16_f32 v3, v16, v17
	v_pk_max_i16 v2, v2, 0
	v_pk_max_i16 v3, v3, 0
	v_dot2c_f32_f16_e32 v140, v2, v133
	v_dot2c_f32_f16_e32 v141, v3, v137
	v_mfma_f32_32x32x16_bf16 v[2:17], v[66:69], v[144:147], 0
	s_nop 1
	v_permlane32_swap_b32_e32 v140, v141
	v_mfma_f32_32x32x16_bf16 v[2:17], v[70:73], v[90:93], v[2:17]
	v_mfma_f32_32x32x16_bf16 v[2:17], v[74:77], v[86:89], v[2:17]
	v_add_f32_e32 v87, v140, v141
	v_cvt_f16_f32_e32 v87, v87
	v_add_u32_e32 v86, 0xffffff40, v127
	v_cmp_le_i32_e32 vcc, v86, v129
	v_ashrrev_i16_e32 v88, 15, v87
	v_bitop3_b16 v87, v88, v87, s50 bitop3:0x36
	v_mfma_f32_32x32x16_bf16 v[2:17], v[78:81], v[82:85], v[2:17]
	v_cndmask_b32_e32 v86, 0, v87, vcc
	v_mov_b32_e32 v82, 0
	v_mov_b32_e32 v83, 0
	ds_write_b16 v250, v86
	ds_read_b128 v[86:89], v151 offset:49152
	ds_read_b128 v[90:93], v150 offset:49152
	ds_read_b128 v[140:143], v149 offset:49152
	ds_read_b128 v[144:147], v148 offset:49152
	s_waitcnt lgkmcnt(0)
	s_nop 2
	v_cvt_pkrtz_f16_f32 v2, v2, v3
	v_cvt_pkrtz_f16_f32 v3, v10, v11
	v_pk_max_i16 v2, v2, 0
	v_pk_max_i16 v3, v3, 0
	v_dot2c_f32_f16_e32 v82, v2, v130
	v_dot2c_f32_f16_e32 v83, v3, v134
	v_cvt_pkrtz_f16_f32 v2, v4, v5
	v_cvt_pkrtz_f16_f32 v3, v12, v13
	v_pk_max_i16 v2, v2, 0
	v_pk_max_i16 v3, v3, 0
	v_dot2c_f32_f16_e32 v82, v2, v131
	v_dot2c_f32_f16_e32 v83, v3, v135
	v_cvt_pkrtz_f16_f32 v2, v6, v7
	v_cvt_pkrtz_f16_f32 v3, v14, v15
	v_pk_max_i16 v2, v2, 0
	v_pk_max_i16 v3, v3, 0
	v_dot2c_f32_f16_e32 v82, v2, v132
	v_dot2c_f32_f16_e32 v83, v3, v136
	v_cvt_pkrtz_f16_f32 v2, v8, v9
	v_cvt_pkrtz_f16_f32 v3, v16, v17
	v_pk_max_i16 v2, v2, 0
	v_pk_max_i16 v3, v3, 0
	v_dot2c_f32_f16_e32 v82, v2, v133
	v_dot2c_f32_f16_e32 v83, v3, v137
	v_mfma_f32_32x32x16_bf16 v[2:17], v[66:69], v[144:147], 0
	v_add_u32_e32 v84, 0xffffff80, v127
	v_cmp_le_i32_e32 vcc, v84, v129
	v_permlane32_swap_b32_e32 v82, v83
	v_add_f32_e32 v82, v82, v83
	v_cvt_f16_f32_e32 v82, v82
	v_ashrrev_i16_e32 v83, 15, v82
	v_mfma_f32_32x32x16_bf16 v[2:17], v[70:73], v[140:143], v[2:17]
	v_bitop3_b16 v82, v83, v82, s50 bitop3:0x36
	v_cndmask_b32_e32 v82, 0, v82, vcc
	ds_write_b16 v250, v82 offset:128
	v_mfma_f32_32x32x16_bf16 v[2:17], v[74:77], v[90:93], v[2:17]
	ds_read_b128 v[82:85], v151 offset:57344
	ds_read_b128 v[90:93], v150 offset:57344
	ds_read_b128 v[140:143], v149 offset:57344
	ds_read_b128 v[144:147], v148 offset:57344
	s_waitcnt lgkmcnt(0)
	v_mfma_f32_32x32x16_bf16 v[2:17], v[78:81], v[86:89], v[2:17]
	v_mov_b32_e32 v86, 0
	v_mov_b32_e32 v87, 0
	s_nop 9
	v_cvt_pkrtz_f16_f32 v2, v2, v3
	v_cvt_pkrtz_f16_f32 v3, v10, v11
	v_pk_max_i16 v2, v2, 0
	v_pk_max_i16 v3, v3, 0
	v_dot2c_f32_f16_e32 v86, v2, v130
	v_dot2c_f32_f16_e32 v87, v3, v134
	v_cvt_pkrtz_f16_f32 v2, v4, v5
	v_cvt_pkrtz_f16_f32 v3, v12, v13
	v_pk_max_i16 v2, v2, 0
	v_pk_max_i16 v3, v3, 0
	v_dot2c_f32_f16_e32 v86, v2, v131
	v_dot2c_f32_f16_e32 v87, v3, v135
	v_cvt_pkrtz_f16_f32 v2, v6, v7
	v_cvt_pkrtz_f16_f32 v3, v14, v15
	v_pk_max_i16 v2, v2, 0
	v_pk_max_i16 v3, v3, 0
	v_dot2c_f32_f16_e32 v86, v2, v132
	v_dot2c_f32_f16_e32 v87, v3, v136
	v_cvt_pkrtz_f16_f32 v2, v8, v9
	v_cvt_pkrtz_f16_f32 v3, v16, v17
	v_pk_max_i16 v2, v2, 0
	v_pk_max_i16 v3, v3, 0
	v_dot2c_f32_f16_e32 v86, v2, v133
	v_dot2c_f32_f16_e32 v87, v3, v137
	v_mfma_f32_32x32x16_bf16 v[2:17], v[66:69], v[144:147], 0
	s_nop 1
	v_permlane32_swap_b32_e32 v86, v87
	v_mfma_f32_32x32x16_bf16 v[2:17], v[70:73], v[140:143], v[2:17]
	v_mfma_f32_32x32x16_bf16 v[2:17], v[74:77], v[90:93], v[2:17]
	v_mfma_f32_32x32x16_bf16 v[2:17], v[78:81], v[82:85], v[2:17]
	v_add_f32_e32 v83, v86, v87
	v_cvt_f16_f32_e32 v83, v83
	v_subrev_u32_e32 v82, 64, v127
	v_cmp_le_i32_e32 vcc, v82, v129
	v_ashrrev_i16_e32 v84, 15, v83
	v_bitop3_b16 v83, v84, v83, s50 bitop3:0x36
	s_nop 5
	v_cvt_pkrtz_f16_f32 v2, v2, v3
	v_pk_max_i16 v2, v2, 0
	v_cvt_pkrtz_f16_f32 v3, v10, v11
	v_mov_b32_e32 v10, 0
	v_pk_max_i16 v3, v3, 0
	v_dot2c_f32_f16_e32 v10, v2, v130
	v_mov_b32_e32 v2, 0
	v_dot2c_f32_f16_e32 v2, v3, v134
	v_cvt_pkrtz_f16_f32 v3, v4, v5
	v_cvt_pkrtz_f16_f32 v4, v12, v13
	v_pk_max_i16 v3, v3, 0
	v_pk_max_i16 v4, v4, 0
	v_dot2c_f32_f16_e32 v10, v3, v131
	v_dot2c_f32_f16_e32 v2, v4, v135
	v_cvt_pkrtz_f16_f32 v3, v6, v7
	v_cvt_pkrtz_f16_f32 v4, v14, v15
	v_pk_max_i16 v3, v3, 0
	v_pk_max_i16 v4, v4, 0
	v_dot2c_f32_f16_e32 v10, v3, v132
	v_dot2c_f32_f16_e32 v2, v4, v136
	v_cvt_pkrtz_f16_f32 v3, v8, v9
	v_cvt_pkrtz_f16_f32 v4, v16, v17
	v_pk_max_i16 v3, v3, 0
	v_pk_max_i16 v4, v4, 0
	v_dot2c_f32_f16_e32 v10, v3, v133
	v_dot2c_f32_f16_e32 v2, v4, v137
	v_cndmask_b32_e32 v82, 0, v83, vcc
	v_cmp_le_i32_e32 vcc, v127, v129
	ds_write_b16 v250, v82 offset:256
	v_permlane32_swap_b32_e32 v10, v2
	v_add_f32_e32 v2, v10, v2
	v_cvt_f16_f32_e32 v2, v2
	v_ashrrev_i16_e32 v3, 15, v2
	v_bitop3_b16 v2, v3, v2, s50 bitop3:0x36
	v_cndmask_b32_e32 v2, 0, v2, vcc
	s_and_b64 vcc, exec, s[8:9]
	ds_write_b16 v250, v2 offset:384
	s_cbranch_vccz .LBB0_1240
	s_cmp_lg_u32 s4, 0
	s_cbranch_scc0 .LBB0_1242
	s_waitcnt vmcnt(0) lgkmcnt(0)
	s_cbranch_execnz .LBB0_1239

.LBB0_3777:
	v_ashrrev_i32_e32 v11, 31, v10
	v_lshlrev_b64 v[6:7], 14, v[10:11]
	v_mov_b32_e32 v11, v54
	v_mov_b32_e32 v12, 0
	v_lshlrev_b32_e32 v2, 4, v11
	v_add_u32_e32 v8, 0x400, v2
	v_ashrrev_i32_e32 v3, 31, v2
	v_ashrrev_i32_e32 v9, 31, v8
	v_lshl_add_u64 v[4:5], v[6:7], 0, v[2:3]
	v_lshl_add_u64 v[6:7], v[6:7], 0, v[8:9]
	v_lshl_add_u64 v[4:5], s[46:47], 0, v[4:5]
	v_lshl_add_u64 v[6:7], s[46:47], 0, v[6:7]
	s_mov_b64 s[8:9], 0
	v_mov_b32_e32 v13, v12
	v_mov_b32_e32 v38, v12
	v_mov_b32_e32 v39, v12
	v_mov_b32_e32 v40, v12
	v_mov_b32_e32 v41, v12
	v_mov_b32_e32 v34, v12
	v_mov_b32_e32 v35, v12
	v_mov_b32_e32 v36, v12
	v_mov_b32_e32 v37, v12
	v_mov_b32_e32 v30, v12
	v_mov_b32_e32 v31, v12
	v_mov_b32_e32 v32, v12
	v_mov_b32_e32 v33, v12
	v_mov_b32_e32 v26, v12
	v_mov_b32_e32 v27, v12
	v_mov_b32_e32 v28, v12
	v_mov_b32_e32 v29, v12
	v_mov_b32_e32 v22, v12
	v_mov_b32_e32 v23, v12
	v_mov_b32_e32 v24, v12
	v_mov_b32_e32 v25, v12
	v_mov_b32_e32 v8, v12
	v_mov_b32_e32 v9, v12
	v_mov_b32_e32 v20, v12
	v_mov_b32_e32 v21, v12
	v_mov_b32_e32 v16, v12
	v_mov_b32_e32 v17, v12
	v_mov_b32_e32 v18, v12
	v_mov_b32_e32 v19, v12
	v_mov_b32_e32 v14, v12
	v_mov_b32_e32 v15, v12
	s_mov_b32 s13, 0
	s_mov_b32 s12, 0x14138c00
	v_lshl_add_u64 v[68:69], v[4:5], 0, s[12:13]
	s_mov_b32 s12, 0x14139c00
	v_lshl_add_u64 v[70:71], v[4:5], 0, s[12:13]
	s_mov_b32 s12, 0x1413ac00
	v_lshl_add_u64 v[72:73], v[4:5], 0, s[12:13]
	s_mov_b32 s12, 0x1413bc00
	v_lshl_add_u64 v[74:75], v[4:5], 0, s[12:13]
	global_load_dwordx4 v[96:99], v[68:69], off
	global_load_dwordx4 v[100:103], v[68:69], off offset:1024
	global_load_dwordx4 v[104:107], v[68:69], off offset:2048
	global_load_dwordx4 v[108:111], v[68:69], off offset:3072
	global_load_dwordx4 v[112:115], v[70:71], off
	global_load_dwordx4 v[116:119], v[70:71], off offset:1024
	global_load_dwordx4 v[120:123], v[70:71], off offset:2048
	global_load_dwordx4 v[124:127], v[70:71], off offset:3072
	global_load_dwordx4 v[128:131], v[72:73], off
	global_load_dwordx4 v[132:135], v[72:73], off offset:1024
	global_load_dwordx4 v[136:139], v[72:73], off offset:2048
	global_load_dwordx4 v[140:143], v[72:73], off offset:3072
	global_load_dwordx4 v[144:147], v[74:75], off
	global_load_dwordx4 v[148:151], v[74:75], off offset:1024
	global_load_dwordx4 v[152:155], v[74:75], off offset:2048
	global_load_dwordx4 v[156:159], v[74:75], off offset:3072
	v_add_u32_e32 v168, s5, v10
	v_ashrrev_i32_e32 v169, 31, v168
	v_lshlrev_b64 v[168:169], 12, v[168:169]
	v_lshl_add_u64 v[168:169], s[62:63], 0, v[168:169]
	v_mov_b32_e32 v170, v2
	v_mov_b32_e32 v171, 0
	v_lshl_add_u64 v[168:169], v[170:171], 0, v[168:169]
	global_load_dwordx4 v[164:167], v[168:169], off
	global_load_dwordx4 v[164:167], v[168:169], off offset:1024
	global_load_dwordx4 v[164:167], v[168:169], off offset:2048
	global_load_dwordx4 v[164:167], v[168:169], off offset:3072
	s_waitcnt vmcnt(19)
	v_cvt_pk_f32_fp8_e32 v[76:77], v96
	v_cvt_pk_f32_fp8_sdwa v[78:79], v96 src0_sel:WORD_1
	v_cvt_pk_f32_fp8_e32 v[80:81], v97
	v_cvt_pk_f32_fp8_sdwa v[82:83], v97 src0_sel:WORD_1
	v_cvt_pk_f32_fp8_e32 v[84:85], v98
	v_cvt_pk_f32_fp8_sdwa v[86:87], v98 src0_sel:WORD_1
	v_cvt_pk_f32_fp8_e32 v[88:89], v99
	v_cvt_pk_f32_fp8_sdwa v[90:91], v99 src0_sel:WORD_1
	v_pk_add_f32 v[38:39], v[38:39], v[76:77]
	v_pk_add_f32 v[40:41], v[40:41], v[78:79]
	v_pk_add_f32 v[34:35], v[34:35], v[80:81]
	v_pk_add_f32 v[36:37], v[36:37], v[82:83]
	v_pk_add_f32 v[30:31], v[30:31], v[84:85]
	v_pk_add_f32 v[32:33], v[32:33], v[86:87]
	v_pk_add_f32 v[26:27], v[26:27], v[88:89]
	v_pk_add_f32 v[28:29], v[28:29], v[90:91]
	s_waitcnt vmcnt(18)
	v_cvt_pk_f32_fp8_e32 v[76:77], v100
	v_cvt_pk_f32_fp8_sdwa v[78:79], v100 src0_sel:WORD_1
	v_cvt_pk_f32_fp8_e32 v[80:81], v101
	v_cvt_pk_f32_fp8_sdwa v[82:83], v101 src0_sel:WORD_1
	v_cvt_pk_f32_fp8_e32 v[84:85], v102
	v_cvt_pk_f32_fp8_sdwa v[86:87], v102 src0_sel:WORD_1
	v_cvt_pk_f32_fp8_e32 v[88:89], v103
	v_cvt_pk_f32_fp8_sdwa v[90:91], v103 src0_sel:WORD_1
	v_pk_add_f32 v[22:23], v[22:23], v[76:77]
	v_pk_add_f32 v[24:25], v[24:25], v[78:79]
	v_pk_add_f32 v[8:9], v[8:9], v[80:81]
	v_pk_add_f32 v[20:21], v[20:21], v[82:83]
	v_pk_add_f32 v[16:17], v[16:17], v[84:85]
	v_pk_add_f32 v[18:19], v[18:19], v[86:87]
	v_pk_add_f32 v[14:15], v[14:15], v[88:89]
	v_pk_add_f32 v[12:13], v[12:13], v[90:91]
	s_waitcnt vmcnt(17)
	v_cvt_pk_f32_fp8_e32 v[76:77], v104
	v_cvt_pk_f32_fp8_sdwa v[78:79], v104 src0_sel:WORD_1
	v_cvt_pk_f32_fp8_e32 v[80:81], v105
	v_cvt_pk_f32_fp8_sdwa v[82:83], v105 src0_sel:WORD_1
	v_cvt_pk_f32_fp8_e32 v[84:85], v106
	v_cvt_pk_f32_fp8_sdwa v[86:87], v106 src0_sel:WORD_1
	v_cvt_pk_f32_fp8_e32 v[88:89], v107
	v_cvt_pk_f32_fp8_sdwa v[90:91], v107 src0_sel:WORD_1
	v_pk_add_f32 v[38:39], v[38:39], v[76:77]
	v_pk_add_f32 v[40:41], v[40:41], v[78:79]
	v_pk_add_f32 v[34:35], v[34:35], v[80:81]
	v_pk_add_f32 v[36:37], v[36:37], v[82:83]
	v_pk_add_f32 v[30:31], v[30:31], v[84:85]
	v_pk_add_f32 v[32:33], v[32:33], v[86:87]
	v_pk_add_f32 v[26:27], v[26:27], v[88:89]
	v_pk_add_f32 v[28:29], v[28:29], v[90:91]
	s_waitcnt vmcnt(16)
	v_cvt_pk_f32_fp8_e32 v[76:77], v108
	v_cvt_pk_f32_fp8_sdwa v[78:79], v108 src0_sel:WORD_1
	v_cvt_pk_f32_fp8_e32 v[80:81], v109
	v_cvt_pk_f32_fp8_sdwa v[82:83], v109 src0_sel:WORD_1
	v_cvt_pk_f32_fp8_e32 v[84:85], v110
	v_cvt_pk_f32_fp8_sdwa v[86:87], v110 src0_sel:WORD_1
	v_cvt_pk_f32_fp8_e32 v[88:89], v111
	v_cvt_pk_f32_fp8_sdwa v[90:91], v111 src0_sel:WORD_1
	v_pk_add_f32 v[22:23], v[22:23], v[76:77]
	v_pk_add_f32 v[24:25], v[24:25], v[78:79]
	v_pk_add_f32 v[8:9], v[8:9], v[80:81]
	v_pk_add_f32 v[20:21], v[20:21], v[82:83]
	v_pk_add_f32 v[16:17], v[16:17], v[84:85]
	v_pk_add_f32 v[18:19], v[18:19], v[86:87]
	v_pk_add_f32 v[14:15], v[14:15], v[88:89]
	v_pk_add_f32 v[12:13], v[12:13], v[90:91]
	s_waitcnt vmcnt(15)
	v_cvt_pk_f32_fp8_e32 v[76:77], v112
	v_cvt_pk_f32_fp8_sdwa v[78:79], v112 src0_sel:WORD_1
	v_cvt_pk_f32_fp8_e32 v[80:81], v113
	v_cvt_pk_f32_fp8_sdwa v[82:83], v113 src0_sel:WORD_1
	v_cvt_pk_f32_fp8_e32 v[84:85], v114
	v_cvt_pk_f32_fp8_sdwa v[86:87], v114 src0_sel:WORD_1
	v_cvt_pk_f32_fp8_e32 v[88:89], v115
	v_cvt_pk_f32_fp8_sdwa v[90:91], v115 src0_sel:WORD_1
	v_pk_add_f32 v[38:39], v[38:39], v[76:77]
	v_pk_add_f32 v[40:41], v[40:41], v[78:79]
	v_pk_add_f32 v[34:35], v[34:35], v[80:81]
	v_pk_add_f32 v[36:37], v[36:37], v[82:83]
	v_pk_add_f32 v[30:31], v[30:31], v[84:85]
	v_pk_add_f32 v[32:33], v[32:33], v[86:87]
	v_pk_add_f32 v[26:27], v[26:27], v[88:89]
	v_pk_add_f32 v[28:29], v[28:29], v[90:91]
	s_waitcnt vmcnt(14)
	v_cvt_pk_f32_fp8_e32 v[76:77], v116
	v_cvt_pk_f32_fp8_sdwa v[78:79], v116 src0_sel:WORD_1
	v_cvt_pk_f32_fp8_e32 v[80:81], v117
	v_cvt_pk_f32_fp8_sdwa v[82:83], v117 src0_sel:WORD_1
	v_cvt_pk_f32_fp8_e32 v[84:85], v118
	v_cvt_pk_f32_fp8_sdwa v[86:87], v118 src0_sel:WORD_1
	v_cvt_pk_f32_fp8_e32 v[88:89], v119
	v_cvt_pk_f32_fp8_sdwa v[90:91], v119 src0_sel:WORD_1
	v_pk_add_f32 v[22:23], v[22:23], v[76:77]
	v_pk_add_f32 v[24:25], v[24:25], v[78:79]
	v_pk_add_f32 v[8:9], v[8:9], v[80:81]
	v_pk_add_f32 v[20:21], v[20:21], v[82:83]
	v_pk_add_f32 v[16:17], v[16:17], v[84:85]
	v_pk_add_f32 v[18:19], v[18:19], v[86:87]
	v_pk_add_f32 v[14:15], v[14:15], v[88:89]
	v_pk_add_f32 v[12:13], v[12:13], v[90:91]
	s_waitcnt vmcnt(13)
	v_cvt_pk_f32_fp8_e32 v[76:77], v120
	v_cvt_pk_f32_fp8_sdwa v[78:79], v120 src0_sel:WORD_1
	v_cvt_pk_f32_fp8_e32 v[80:81], v121
	v_cvt_pk_f32_fp8_sdwa v[82:83], v121 src0_sel:WORD_1
	v_cvt_pk_f32_fp8_e32 v[84:85], v122
	v_cvt_pk_f32_fp8_sdwa v[86:87], v122 src0_sel:WORD_1
	v_cvt_pk_f32_fp8_e32 v[88:89], v123
	v_cvt_pk_f32_fp8_sdwa v[90:91], v123 src0_sel:WORD_1
	v_pk_add_f32 v[38:39], v[38:39], v[76:77]
	v_pk_add_f32 v[40:41], v[40:41], v[78:79]
	v_pk_add_f32 v[34:35], v[34:35], v[80:81]
	v_pk_add_f32 v[36:37], v[36:37], v[82:83]
	v_pk_add_f32 v[30:31], v[30:31], v[84:85]
	v_pk_add_f32 v[32:33], v[32:33], v[86:87]
	v_pk_add_f32 v[26:27], v[26:27], v[88:89]
	v_pk_add_f32 v[28:29], v[28:29], v[90:91]
	s_waitcnt vmcnt(12)
	v_cvt_pk_f32_fp8_e32 v[76:77], v124
	v_cvt_pk_f32_fp8_sdwa v[78:79], v124 src0_sel:WORD_1
	v_cvt_pk_f32_fp8_e32 v[80:81], v125
	v_cvt_pk_f32_fp8_sdwa v[82:83], v125 src0_sel:WORD_1
	v_cvt_pk_f32_fp8_e32 v[84:85], v126
	v_cvt_pk_f32_fp8_sdwa v[86:87], v126 src0_sel:WORD_1
	v_cvt_pk_f32_fp8_e32 v[88:89], v127
	v_cvt_pk_f32_fp8_sdwa v[90:91], v127 src0_sel:WORD_1
	v_pk_add_f32 v[22:23], v[22:23], v[76:77]
	v_pk_add_f32 v[24:25], v[24:25], v[78:79]
	v_pk_add_f32 v[8:9], v[8:9], v[80:81]
	v_pk_add_f32 v[20:21], v[20:21], v[82:83]
	v_pk_add_f32 v[16:17], v[16:17], v[84:85]
	v_pk_add_f32 v[18:19], v[18:19], v[86:87]
	v_pk_add_f32 v[14:15], v[14:15], v[88:89]
	v_pk_add_f32 v[12:13], v[12:13], v[90:91]
	s_waitcnt vmcnt(11)
	v_cvt_pk_f32_fp8_e32 v[76:77], v128
	v_cvt_pk_f32_fp8_sdwa v[78:79], v128 src0_sel:WORD_1
	v_cvt_pk_f32_fp8_e32 v[80:81], v129
	v_cvt_pk_f32_fp8_sdwa v[82:83], v129 src0_sel:WORD_1
	v_cvt_pk_f32_fp8_e32 v[84:85], v130
	v_cvt_pk_f32_fp8_sdwa v[86:87], v130 src0_sel:WORD_1
	v_cvt_pk_f32_fp8_e32 v[88:89], v131
	v_cvt_pk_f32_fp8_sdwa v[90:91], v131 src0_sel:WORD_1
	v_pk_add_f32 v[38:39], v[38:39], v[76:77]
	v_pk_add_f32 v[40:41], v[40:41], v[78:79]
	v_pk_add_f32 v[34:35], v[34:35], v[80:81]
	v_pk_add_f32 v[36:37], v[36:37], v[82:83]
	v_pk_add_f32 v[30:31], v[30:31], v[84:85]
	v_pk_add_f32 v[32:33], v[32:33], v[86:87]
	v_pk_add_f32 v[26:27], v[26:27], v[88:89]
	v_pk_add_f32 v[28:29], v[28:29], v[90:91]
	s_waitcnt vmcnt(10)
	v_cvt_pk_f32_fp8_e32 v[76:77], v132
	v_cvt_pk_f32_fp8_sdwa v[78:79], v132 src0_sel:WORD_1
	v_cvt_pk_f32_fp8_e32 v[80:81], v133
	v_cvt_pk_f32_fp8_sdwa v[82:83], v133 src0_sel:WORD_1
	v_cvt_pk_f32_fp8_e32 v[84:85], v134
	v_cvt_pk_f32_fp8_sdwa v[86:87], v134 src0_sel:WORD_1
	v_cvt_pk_f32_fp8_e32 v[88:89], v135
	v_cvt_pk_f32_fp8_sdwa v[90:91], v135 src0_sel:WORD_1
	v_pk_add_f32 v[22:23], v[22:23], v[76:77]
	v_pk_add_f32 v[24:25], v[24:25], v[78:79]
	v_pk_add_f32 v[8:9], v[8:9], v[80:81]
	v_pk_add_f32 v[20:21], v[20:21], v[82:83]
	v_pk_add_f32 v[16:17], v[16:17], v[84:85]
	v_pk_add_f32 v[18:19], v[18:19], v[86:87]
	v_pk_add_f32 v[14:15], v[14:15], v[88:89]
	v_pk_add_f32 v[12:13], v[12:13], v[90:91]
	s_waitcnt vmcnt(9)
	v_cvt_pk_f32_fp8_e32 v[76:77], v136
	v_cvt_pk_f32_fp8_sdwa v[78:79], v136 src0_sel:WORD_1
	v_cvt_pk_f32_fp8_e32 v[80:81], v137
	v_cvt_pk_f32_fp8_sdwa v[82:83], v137 src0_sel:WORD_1
	v_cvt_pk_f32_fp8_e32 v[84:85], v138
	v_cvt_pk_f32_fp8_sdwa v[86:87], v138 src0_sel:WORD_1
	v_cvt_pk_f32_fp8_e32 v[88:89], v139
	v_cvt_pk_f32_fp8_sdwa v[90:91], v139 src0_sel:WORD_1
	v_pk_add_f32 v[38:39], v[38:39], v[76:77]
	v_pk_add_f32 v[40:41], v[40:41], v[78:79]
	v_pk_add_f32 v[34:35], v[34:35], v[80:81]
	v_pk_add_f32 v[36:37], v[36:37], v[82:83]
	v_pk_add_f32 v[30:31], v[30:31], v[84:85]
	v_pk_add_f32 v[32:33], v[32:33], v[86:87]
	v_pk_add_f32 v[26:27], v[26:27], v[88:89]
	v_pk_add_f32 v[28:29], v[28:29], v[90:91]
	s_waitcnt vmcnt(8)
	v_cvt_pk_f32_fp8_e32 v[76:77], v140
	v_cvt_pk_f32_fp8_sdwa v[78:79], v140 src0_sel:WORD_1
	v_cvt_pk_f32_fp8_e32 v[80:81], v141
	v_cvt_pk_f32_fp8_sdwa v[82:83], v141 src0_sel:WORD_1
	v_cvt_pk_f32_fp8_e32 v[84:85], v142
	v_cvt_pk_f32_fp8_sdwa v[86:87], v142 src0_sel:WORD_1
	v_cvt_pk_f32_fp8_e32 v[88:89], v143
	v_cvt_pk_f32_fp8_sdwa v[90:91], v143 src0_sel:WORD_1
	v_pk_add_f32 v[22:23], v[22:23], v[76:77]
	v_pk_add_f32 v[24:25], v[24:25], v[78:79]
	v_pk_add_f32 v[8:9], v[8:9], v[80:81]
	v_pk_add_f32 v[20:21], v[20:21], v[82:83]
	v_pk_add_f32 v[16:17], v[16:17], v[84:85]
	v_pk_add_f32 v[18:19], v[18:19], v[86:87]
	v_pk_add_f32 v[14:15], v[14:15], v[88:89]
	v_pk_add_f32 v[12:13], v[12:13], v[90:91]
	s_waitcnt vmcnt(7)
	v_cvt_pk_f32_fp8_e32 v[76:77], v144
	v_cvt_pk_f32_fp8_sdwa v[78:79], v144 src0_sel:WORD_1
	v_cvt_pk_f32_fp8_e32 v[80:81], v145
	v_cvt_pk_f32_fp8_sdwa v[82:83], v145 src0_sel:WORD_1
	v_cvt_pk_f32_fp8_e32 v[84:85], v146
	v_cvt_pk_f32_fp8_sdwa v[86:87], v146 src0_sel:WORD_1
	v_cvt_pk_f32_fp8_e32 v[88:89], v147
	v_cvt_pk_f32_fp8_sdwa v[90:91], v147 src0_sel:WORD_1
	v_pk_add_f32 v[38:39], v[38:39], v[76:77]
	v_pk_add_f32 v[40:41], v[40:41], v[78:79]
	v_pk_add_f32 v[34:35], v[34:35], v[80:81]
	v_pk_add_f32 v[36:37], v[36:37], v[82:83]
	v_pk_add_f32 v[30:31], v[30:31], v[84:85]
	v_pk_add_f32 v[32:33], v[32:33], v[86:87]
	v_pk_add_f32 v[26:27], v[26:27], v[88:89]
	v_pk_add_f32 v[28:29], v[28:29], v[90:91]
	s_waitcnt vmcnt(6)
	v_cvt_pk_f32_fp8_e32 v[76:77], v148
	v_cvt_pk_f32_fp8_sdwa v[78:79], v148 src0_sel:WORD_1
	v_cvt_pk_f32_fp8_e32 v[80:81], v149
	v_cvt_pk_f32_fp8_sdwa v[82:83], v149 src0_sel:WORD_1
	v_cvt_pk_f32_fp8_e32 v[84:85], v150
	v_cvt_pk_f32_fp8_sdwa v[86:87], v150 src0_sel:WORD_1
	v_cvt_pk_f32_fp8_e32 v[88:89], v151
	v_cvt_pk_f32_fp8_sdwa v[90:91], v151 src0_sel:WORD_1
	v_pk_add_f32 v[22:23], v[22:23], v[76:77]
	v_pk_add_f32 v[24:25], v[24:25], v[78:79]
	v_pk_add_f32 v[8:9], v[8:9], v[80:81]
	v_pk_add_f32 v[20:21], v[20:21], v[82:83]
	v_pk_add_f32 v[16:17], v[16:17], v[84:85]
	v_pk_add_f32 v[18:19], v[18:19], v[86:87]
	v_pk_add_f32 v[14:15], v[14:15], v[88:89]
	v_pk_add_f32 v[12:13], v[12:13], v[90:91]
	s_waitcnt vmcnt(5)
	v_cvt_pk_f32_fp8_e32 v[76:77], v152
	v_cvt_pk_f32_fp8_sdwa v[78:79], v152 src0_sel:WORD_1
	v_cvt_pk_f32_fp8_e32 v[80:81], v153
	v_cvt_pk_f32_fp8_sdwa v[82:83], v153 src0_sel:WORD_1
	v_cvt_pk_f32_fp8_e32 v[84:85], v154
	v_cvt_pk_f32_fp8_sdwa v[86:87], v154 src0_sel:WORD_1
	v_cvt_pk_f32_fp8_e32 v[88:89], v155
	v_cvt_pk_f32_fp8_sdwa v[90:91], v155 src0_sel:WORD_1
	v_pk_add_f32 v[38:39], v[38:39], v[76:77]
	v_pk_add_f32 v[40:41], v[40:41], v[78:79]
	v_pk_add_f32 v[34:35], v[34:35], v[80:81]
	v_pk_add_f32 v[36:37], v[36:37], v[82:83]
	v_pk_add_f32 v[30:31], v[30:31], v[84:85]
	v_pk_add_f32 v[32:33], v[32:33], v[86:87]
	v_pk_add_f32 v[26:27], v[26:27], v[88:89]
	v_pk_add_f32 v[28:29], v[28:29], v[90:91]
	s_waitcnt vmcnt(4)
	v_cvt_pk_f32_fp8_e32 v[76:77], v156
	v_cvt_pk_f32_fp8_sdwa v[78:79], v156 src0_sel:WORD_1
	v_cvt_pk_f32_fp8_e32 v[80:81], v157
	v_cvt_pk_f32_fp8_sdwa v[82:83], v157 src0_sel:WORD_1
	v_cvt_pk_f32_fp8_e32 v[84:85], v158
	v_cvt_pk_f32_fp8_sdwa v[86:87], v158 src0_sel:WORD_1
	v_cvt_pk_f32_fp8_e32 v[88:89], v159
	v_cvt_pk_f32_fp8_sdwa v[90:91], v159 src0_sel:WORD_1
	v_pk_add_f32 v[22:23], v[22:23], v[76:77]
	v_pk_add_f32 v[24:25], v[24:25], v[78:79]
	v_pk_add_f32 v[8:9], v[8:9], v[80:81]
	v_pk_add_f32 v[20:21], v[20:21], v[82:83]
	v_pk_add_f32 v[16:17], v[16:17], v[84:85]
	v_pk_add_f32 v[18:19], v[18:19], v[86:87]
	v_pk_add_f32 v[14:15], v[14:15], v[88:89]
	v_pk_add_f32 v[12:13], v[12:13], v[90:91]
	v_and_b32_e32 v3, 0xffffe000, v10
	v_add_u32_e32 v57, 0, v3
	v_lshlrev_b32_e32 v3, 3, v11
	v_add_u32_e32 v46, s5, v10
	v_and_b32_e32 v11, 24, v3
	v_and_b32_e32 v3, 0xffffff00, v2
	v_lshrrev_b32_e32 v2, 1, v2
	s_movk_i32 s8, 0x60
	v_ashrrev_i32_e32 v47, 31, v46
	v_and_or_b32 v55, v2, s8, v3
	v_lshlrev_b64 v[4:5], 12, v[46:47]
	v_or_b32_e32 v42, v55, v11
	v_lshl_add_u64 v[4:5], s[62:63], 0, v[4:5]
	v_lshlrev_b32_e32 v56, 2, v42
	v_ashrrev_i32_e32 v43, 31, v42
	v_add_u32_e32 v62, v57, v56
	v_lshl_add_u64 v[2:3], v[42:43], 1, v[4:5]
	ds_read_b128 v[48:51], v62
	ds_read_b128 v[58:61], v62 offset:16
	global_load_dwordx2 v[2:3], v[2:3], off
	v_readlane_b32 s12, v253, 2
	v_readlane_b32 s26, v253, 16
	v_readlane_b32 s27, v253, 17
	s_mov_b32 s8, 0x800000
	v_add_u32_e32 v10, s52, v10
	v_readlane_b32 s13, v253, 3
	v_readlane_b32 s14, v253, 4
	v_readlane_b32 s15, v253, 5
	v_readlane_b32 s16, v253, 6
	v_readlane_b32 s17, v253, 7
	v_readlane_b32 s18, v253, 8
	v_readlane_b32 s19, v253, 9
	v_readlane_b32 s20, v253, 10
	v_readlane_b32 s21, v253, 11
	v_readlane_b32 s22, v253, 12
	v_readlane_b32 s23, v253, 13
	v_readlane_b32 s24, v253, 14
	v_readlane_b32 s25, v253, 15
	s_waitcnt vmcnt(0)
	v_lshlrev_b32_e32 v6, 16, v2
	v_and_b32_e32 v7, 0xffff0000, v2
	v_lshlrev_b32_e32 v2, 16, v3
	v_and_b32_e32 v3, 0xffff0000, v3
	s_waitcnt lgkmcnt(1)
	v_pk_fma_f32 v[40:41], v[40:41], v[50:51], v[2:3]
	v_pk_fma_f32 v[44:45], v[38:39], v[48:49], v[6:7]
	v_add_f32_e32 v3, v40, v41
	v_add_f32_e32 v2, v44, v45
	v_add_f32_e32 v2, v2, v3
	v_ashrrev_i32_e32 v39, 31, v55
	v_mov_b32_e32 v38, v42
	v_add_f32_e32 v50, 0, v2
	v_lshl_add_u64 v[2:3], v[38:39], 1, v[4:5]
	global_load_dwordx2 v[6:7], v[2:3], off offset:8
	v_add_u32_e32 v55, 0x400, v55
	s_waitcnt vmcnt(0)
	v_lshlrev_b32_e32 v48, 16, v6
	v_and_b32_e32 v49, 0xffff0000, v6
	v_lshlrev_b32_e32 v6, 16, v7
	v_and_b32_e32 v7, 0xffff0000, v7
	s_waitcnt lgkmcnt(0)
	v_pk_fma_f32 v[36:37], v[36:37], v[60:61], v[6:7]
	v_pk_fma_f32 v[34:35], v[34:35], v[58:59], v[48:49]
	global_load_dwordx4 v[58:61], v[2:3], off offset:256
	v_add_f32_e32 v6, v34, v35
	v_add_f32_e32 v7, v36, v37
	v_add_f32_e32 v6, v6, v7
	v_add_f32_e32 v52, v50, v6
	ds_read_b128 v[48:51], v62 offset:512
	s_waitcnt vmcnt(0)
	v_lshlrev_b32_e32 v2, 16, v58
	v_and_b32_e32 v3, 0xffff0000, v58
	v_lshlrev_b32_e32 v6, 16, v59
	v_and_b32_e32 v7, 0xffff0000, v59
	s_waitcnt lgkmcnt(0)
	v_pk_fma_f32 v[32:33], v[32:33], v[50:51], v[6:7]
	v_pk_fma_f32 v[30:31], v[30:31], v[48:49], v[2:3]
	v_add_f32_e32 v3, v32, v33
	v_add_f32_e32 v2, v30, v31
	v_add_f32_e32 v2, v2, v3
	v_add_f32_e32 v58, v52, v2
	ds_read_b128 v[50:53], v62 offset:528
	v_lshlrev_b32_e32 v2, 16, v60
	v_and_b32_e32 v3, 0xffff0000, v60
	v_lshlrev_b32_e32 v6, 16, v61
	v_and_b32_e32 v7, 0xffff0000, v61
	s_waitcnt lgkmcnt(0)
	v_pk_fma_f32 v[48:49], v[28:29], v[52:53], v[6:7]
	v_pk_fma_f32 v[28:29], v[26:27], v[50:51], v[2:3]
	v_add_f32_e32 v3, v48, v49
	v_add_f32_e32 v2, v28, v29
	v_or_b32_e32 v26, v55, v11
	v_add_f32_e32 v2, v2, v3
	v_ashrrev_i32_e32 v27, 31, v26
	v_add_f32_e32 v58, v58, v2
	v_lshl_add_u64 v[2:3], v[26:27], 1, v[4:5]
	global_load_dwordx2 v[2:3], v[2:3], off
	ds_read_b128 v[50:53], v62 offset:4096
	v_or_b32_e32 v11, 16, v56
	s_waitcnt vmcnt(0)
	v_lshlrev_b32_e32 v6, 16, v2
	v_and_b32_e32 v7, 0xffff0000, v2
	v_lshlrev_b32_e32 v2, 16, v3
	v_and_b32_e32 v3, 0xffff0000, v3
	s_waitcnt lgkmcnt(0)
	v_pk_fma_f32 v[52:53], v[24:25], v[52:53], v[2:3]
	v_pk_fma_f32 v[50:51], v[22:23], v[50:51], v[6:7]
	v_add_f32_e32 v3, v52, v53
	v_add_f32_e32 v2, v50, v51
	v_add_f32_e32 v2, v2, v3
	v_ashrrev_i32_e32 v23, 31, v55
	v_mov_b32_e32 v22, v26
	v_add_f32_e32 v62, v58, v2
	v_add_u32_e32 v2, v57, v11
	v_lshl_add_u64 v[6:7], v[22:23], 1, v[4:5]
	ds_read_b128 v[58:61], v2 offset:4096
	global_load_dwordx2 v[2:3], v[6:7], off offset:8
	v_or_b32_e32 v55, 0x200, v56
	v_add_u32_e32 v11, 0, v11
	s_waitcnt vmcnt(0)
	v_lshlrev_b32_e32 v4, 16, v2
	v_and_b32_e32 v5, 0xffff0000, v2
	v_lshlrev_b32_e32 v2, 16, v3
	v_and_b32_e32 v3, 0xffff0000, v3
	s_waitcnt lgkmcnt(0)
	v_pk_fma_f32 v[24:25], v[20:21], v[60:61], v[2:3]
	v_pk_fma_f32 v[20:21], v[8:9], v[58:59], v[4:5]
	global_load_dwordx4 v[6:9], v[6:7], off offset:256
	v_add_f32_e32 v2, v20, v21
	v_add_f32_e32 v3, v24, v25
	v_add_f32_e32 v2, v2, v3
	v_add_f32_e32 v60, v62, v2
	v_add_u32_e32 v2, v57, v55
	ds_read_b128 v[2:5], v2 offset:4096
	s_waitcnt vmcnt(0)
	v_lshlrev_b32_e32 v58, 16, v6
	v_and_b32_e32 v59, 0xffff0000, v6
	v_lshlrev_b32_e32 v6, 16, v7
	v_and_b32_e32 v7, 0xffff0000, v7
	s_waitcnt lgkmcnt(0)
	v_pk_fma_f32 v[4:5], v[18:19], v[4:5], v[6:7]
	v_pk_fma_f32 v[2:3], v[16:17], v[2:3], v[58:59]
	v_add_f32_e32 v7, v4, v5
	v_add_f32_e32 v6, v2, v3
	v_add_f32_e32 v6, v6, v7
	v_or_b32_e32 v16, 0x210, v56
	v_add_f32_e32 v17, v60, v6
	v_add_u32_e32 v6, v57, v16
	ds_read_b128 v[58:61], v6 offset:4096
	v_lshlrev_b32_e32 v18, 16, v8
	v_and_b32_e32 v19, 0xffff0000, v8
	v_lshlrev_b32_e32 v6, 16, v9
	v_and_b32_e32 v7, 0xffff0000, v9
	s_waitcnt lgkmcnt(0)
	v_pk_fma_f32 v[6:7], v[12:13], v[60:61], v[6:7]
	v_pk_fma_f32 v[8:9], v[14:15], v[58:59], v[18:19]
	v_add_f32_e32 v13, v6, v7
	v_add_f32_e32 v12, v8, v9
	v_add_f32_e32 v12, v12, v13
	v_add_f32_e32 v12, v17, v12
	s_nop 1
	v_add_f32_dpp v12, v12, v12 quad_perm:[1,0,3,2] row_mask:0xf bank_mask:0xf bound_ctrl:1
	s_nop 1
	v_add_f32_dpp v12, v12, v12 quad_perm:[2,3,0,1] row_mask:0xf bank_mask:0xf bound_ctrl:1
	s_nop 1
	v_add_f32_dpp v12, v12, v12 row_half_mirror row_mask:0xf bank_mask:0xf bound_ctrl:1
	s_nop 1
	v_add_f32_dpp v12, v12, v12 row_mirror row_mask:0xf bank_mask:0xf bound_ctrl:1
	v_mov_b32_e32 v13, v12
	s_nop 1
	v_permlane16_swap_b32_e32 v12, v13
	v_add_f32_e32 v12, v12, v13
	v_mov_b32_e32 v13, v12
	s_nop 1
	v_permlane32_swap_b32_e32 v12, v13
	v_add_f32_e32 v12, v12, v13
	v_fmac_f32_e32 v41, 0xba000000, v12
	v_fmac_f32_e32 v45, 0xba000000, v12
	v_fmamk_f32 v40, v12, 0xba000000, v40
	v_fmamk_f32 v44, v12, 0xba000000, v44
	v_mul_f32_e32 v13, v45, v45
	v_mul_f32_e32 v14, v41, v41
	v_fmac_f32_e32 v13, v44, v44
	v_fmac_f32_e32 v14, v40, v40
	v_fmac_f32_e32 v37, 0xba000000, v12
	v_fmac_f32_e32 v35, 0xba000000, v12
	v_add_f32_e32 v13, v13, v14
	v_fmamk_f32 v36, v12, 0xba000000, v36
	v_fmamk_f32 v34, v12, 0xba000000, v34
	v_mul_f32_e32 v14, v35, v35
	v_mul_f32_e32 v15, v37, v37
	v_fmac_f32_e32 v14, v34, v34
	v_fmac_f32_e32 v15, v36, v36
	v_add_f32_e32 v14, v14, v15
	v_fmac_f32_e32 v33, 0xba000000, v12
	v_fmac_f32_e32 v31, 0xba000000, v12
	v_add_f32_e32 v13, v13, v14
	v_fmamk_f32 v32, v12, 0xba000000, v32
	v_fmamk_f32 v30, v12, 0xba000000, v30
	v_mul_f32_e32 v14, v31, v31
	v_mul_f32_e32 v15, v33, v33
	v_fmac_f32_e32 v14, v30, v30
	v_fmac_f32_e32 v15, v32, v32
	v_add_f32_e32 v14, v14, v15
	v_fmac_f32_e32 v49, 0xba000000, v12
	v_fmac_f32_e32 v29, 0xba000000, v12
	v_add_f32_e32 v13, v14, v13
	v_fmamk_f32 v48, v12, 0xba000000, v48
	v_fmamk_f32 v28, v12, 0xba000000, v28
	v_mul_f32_e32 v14, v29, v29
	v_mul_f32_e32 v15, v49, v49
	v_fmac_f32_e32 v14, v28, v28
	v_fmac_f32_e32 v15, v48, v48
	v_add_f32_e32 v14, v14, v15
	v_fmac_f32_e32 v53, 0xba000000, v12
	v_fmac_f32_e32 v51, 0xba000000, v12
	v_add_f32_e32 v13, v14, v13
	v_fmamk_f32 v52, v12, 0xba000000, v52
	v_fmamk_f32 v50, v12, 0xba000000, v50
	v_mul_f32_e32 v14, v51, v51
	v_mul_f32_e32 v15, v53, v53
	v_fmac_f32_e32 v14, v50, v50
	v_fmac_f32_e32 v15, v52, v52
	v_add_f32_e32 v14, v14, v15
	v_fmac_f32_e32 v25, 0xba000000, v12
	v_fmac_f32_e32 v21, 0xba000000, v12
	v_add_f32_e32 v13, v14, v13
	v_fmamk_f32 v24, v12, 0xba000000, v24
	v_fmamk_f32 v20, v12, 0xba000000, v20
	v_mul_f32_e32 v14, v21, v21
	v_mul_f32_e32 v15, v25, v25
	v_fmac_f32_e32 v14, v20, v20
	v_fmac_f32_e32 v15, v24, v24
	v_add_f32_e32 v14, v14, v15
	v_fmac_f32_e32 v5, 0xba000000, v12
	v_fmac_f32_e32 v3, 0xba000000, v12
	v_add_f32_e32 v13, v14, v13
	v_fmamk_f32 v4, v12, 0xba000000, v4
	v_fmamk_f32 v2, v12, 0xba000000, v2
	v_mul_f32_e32 v14, v3, v3
	v_mul_f32_e32 v15, v5, v5
	v_fmac_f32_e32 v14, v2, v2
	v_fmac_f32_e32 v15, v4, v4
	v_add_f32_e32 v14, v14, v15
	v_fmac_f32_e32 v7, 0xba000000, v12
	v_fmac_f32_e32 v9, 0xba000000, v12
	v_add_f32_e32 v13, v14, v13
	v_fmamk_f32 v6, v12, 0xba000000, v6
	v_fmamk_f32 v8, v12, 0xba000000, v8
	v_mul_f32_e32 v12, v9, v9
	v_mul_f32_e32 v14, v7, v7
	v_fmac_f32_e32 v12, v8, v8
	v_fmac_f32_e32 v14, v6, v6
	v_add_f32_e32 v12, v12, v14
	v_add_f32_e32 v17, v12, v13
	v_lshlrev_b64 v[12:13], 13, v[46:47]
	v_lshl_add_u64 v[14:15], s[26:27], 0, v[12:13]
	s_nop 0
	v_add_f32_dpp v12, v17, v17 quad_perm:[1,0,3,2] row_mask:0xf bank_mask:0xf bound_ctrl:1
	s_nop 1
	v_add_f32_dpp v12, v12, v12 quad_perm:[2,3,0,1] row_mask:0xf bank_mask:0xf bound_ctrl:1
	s_nop 1
	v_add_f32_dpp v12, v12, v12 row_half_mirror row_mask:0xf bank_mask:0xf bound_ctrl:1
	s_nop 1
	v_add_f32_dpp v12, v12, v12 row_mirror row_mask:0xf bank_mask:0xf bound_ctrl:1
	v_mov_b32_e32 v13, v12
	s_nop 1
	v_permlane16_swap_b32_e32 v12, v13
	v_add_f32_e32 v12, v12, v13
	v_mov_b32_e32 v13, v12
	s_nop 1
	v_permlane32_swap_b32_e32 v12, v13
	v_add_f32_e32 v12, v12, v13
	v_fmamk_f32 v12, v12, 0x3a000000, v212
	v_cmp_gt_f32_e32 vcc, s8, v12
	v_mul_f32_e32 v13, 0x4b800000, v12
	s_movk_i32 s8, 0x3fff
	v_cndmask_b32_e32 v12, v12, v13, vcc
	v_rsq_f32_e32 v12, v12
	s_nop 0
	v_mul_f32_e32 v13, 0x45800000, v12
	v_cndmask_b32_e32 v12, v12, v13, vcc
	v_pk_mul_f32 v[18:19], v[44:45], v[12:13] op_sel_hi:[1,0]
	v_pk_mul_f32 v[40:41], v[40:41], v[12:13] op_sel_hi:[1,0]
	v_add_u32_e32 v13, 0, v56
	ds_read_b128 v[44:47], v13 offset:16384
	ds_read_b128 v[56:59], v13 offset:24576
	v_cmp_lt_i32_e32 vcc, s8, v10
	s_or_b64 s[2:3], vcc, s[2:3]
	s_waitcnt lgkmcnt(0)
	v_pk_fma_f32 v[46:47], v[46:47], v[40:41], v[58:59]
	v_pk_fma_f32 v[44:45], v[44:45], v[18:19], v[56:57]
	v_lshl_add_u64 v[18:19], v[42:43], 2, v[14:15]
	global_store_dwordx4 v[18:19], v[44:47], off
	v_pk_mul_f32 v[18:19], v[36:37], v[12:13] op_sel_hi:[1,0]
	s_nop 0
	v_pk_mul_f32 v[44:45], v[34:35], v[12:13] op_sel_hi:[1,0]
	ds_read_b128 v[34:37], v13 offset:16400
	ds_read_b128 v[40:43], v13 offset:24592
	s_waitcnt lgkmcnt(0)
	v_pk_fma_f32 v[34:35], v[34:35], v[44:45], v[40:41]
	v_pk_fma_f32 v[36:37], v[36:37], v[18:19], v[42:43]
	v_lshl_add_u64 v[18:19], v[38:39], 2, v[14:15]
	global_store_dwordx4 v[18:19], v[34:37], off offset:16
	v_pk_mul_f32 v[38:39], v[32:33], v[12:13] op_sel_hi:[1,0]
	v_pk_mul_f32 v[40:41], v[30:31], v[12:13] op_sel_hi:[1,0]
	ds_read_b128 v[30:33], v13 offset:16896
	ds_read_b128 v[34:37], v13 offset:25088
	s_waitcnt lgkmcnt(0)
	v_pk_fma_f32 v[30:31], v[30:31], v[40:41], v[34:35]
	v_pk_fma_f32 v[32:33], v[32:33], v[38:39], v[36:37]
	global_store_dwordx4 v[18:19], v[30:33], off offset:512
	v_pk_mul_f32 v[38:39], v[28:29], v[12:13] op_sel_hi:[1,0]
	ds_read_b128 v[28:31], v13 offset:16912
	ds_read_b128 v[32:35], v13 offset:25104
	v_pk_mul_f32 v[36:37], v[48:49], v[12:13] op_sel_hi:[1,0]
	s_waitcnt lgkmcnt(0)
	v_pk_fma_f32 v[28:29], v[28:29], v[38:39], v[32:33]
	v_pk_fma_f32 v[30:31], v[30:31], v[36:37], v[34:35]
	global_store_dwordx4 v[18:19], v[28:31], off offset:528
	ds_read_b128 v[28:31], v13 offset:20480
	ds_read_b128 v[32:35], v13 offset:28672
	v_pk_mul_f32 v[18:19], v[52:53], v[12:13] op_sel_hi:[1,0]
	v_pk_mul_f32 v[36:37], v[50:51], v[12:13] op_sel_hi:[1,0]
	s_waitcnt lgkmcnt(0)
	v_pk_fma_f32 v[30:31], v[18:19], v[30:31], v[34:35]
	v_pk_fma_f32 v[28:29], v[36:37], v[28:29], v[32:33]
	v_lshl_add_u64 v[18:19], v[26:27], 2, v[14:15]
	global_store_dwordx4 v[18:19], v[28:31], off
	v_lshl_add_u64 v[14:15], v[22:23], 2, v[14:15]
	v_pk_mul_f32 v[22:23], v[4:5], v[12:13] op_sel_hi:[1,0]
	v_pk_mul_f32 v[28:29], v[24:25], v[12:13] op_sel_hi:[1,0]
	v_pk_mul_f32 v[30:31], v[20:21], v[12:13] op_sel_hi:[1,0]
	ds_read_b128 v[18:21], v11 offset:20480
	ds_read_b128 v[24:27], v11 offset:28672
	v_add_u32_e32 v11, 0, v55
	s_waitcnt lgkmcnt(0)
	v_pk_fma_f32 v[18:19], v[30:31], v[18:19], v[24:25]
	v_pk_fma_f32 v[20:21], v[28:29], v[20:21], v[26:27]
	global_store_dwordx4 v[14:15], v[18:21], off offset:16
	v_pk_mul_f32 v[24:25], v[2:3], v[12:13] op_sel_hi:[1,0]
	ds_read_b128 v[2:5], v11 offset:20480
	ds_read_b128 v[18:21], v11 offset:28672
	s_waitcnt lgkmcnt(0)
	v_pk_fma_f32 v[2:3], v[24:25], v[2:3], v[18:19]
	v_pk_fma_f32 v[4:5], v[22:23], v[4:5], v[20:21]
	global_store_dwordx4 v[14:15], v[2:5], off offset:512
	v_pk_mul_f32 v[18:19], v[6:7], v[12:13] op_sel_hi:[1,0]
	v_add_u32_e32 v6, 0, v16
	v_pk_mul_f32 v[12:13], v[8:9], v[12:13] op_sel_hi:[1,0]
	ds_read_b128 v[2:5], v6 offset:20480
	ds_read_b128 v[6:9], v6 offset:28672
	s_waitcnt lgkmcnt(0)
	v_pk_fma_f32 v[2:3], v[12:13], v[2:3], v[6:7]
	v_pk_fma_f32 v[4:5], v[18:19], v[4:5], v[8:9]
	global_store_dwordx4 v[14:15], v[2:5], off offset:528
	s_andn2_b64 exec, exec, s[2:3]
	s_cbranch_execnz .LBB0_3777
	s_branch .LBB0_3758
